# baseline (speedup 1.0000x reference)
.Lg_nostag:
	v_add_u32_e32 v6, s33, v5
	ds_read_b128 v[72:75], v6 offset:0
	ds_read_b128 v[76:79], v6 offset:2048
	ds_read_b128 v[80:83], v6 offset:4096
	ds_read_b128 v[84:87], v6 offset:6144
	ds_read_b128 v[88:91], v4 offset:0
	ds_read_b128 v[92:95], v4 offset:2048
	ds_read_b128 v[96:99], v4 offset:4096
	ds_read_b128 v[100:103], v4 offset:6144
	ds_read_b128 v[104:107], v4 offset:8192
	ds_read_b128 v[108:111], v4 offset:10240
	ds_read_b128 v[112:115], v4 offset:12288
	ds_read_b128 v[116:119], v4 offset:14336
	s_waitcnt vmcnt(18)
	v_cvt_pk_bf16_f32 v40, v40, v41
	v_cvt_pk_bf16_f32 v41, v42, v43
	v_cvt_pk_bf16_f32 v44, v44, v45
	v_cvt_pk_bf16_f32 v45, v46, v47
	ds_write2st64_b64 v3, v[40:41], v[44:45] offset0:64 offset1:72
	s_waitcnt vmcnt(16)
	v_cvt_pk_bf16_f32 v48, v48, v49
	v_cvt_pk_bf16_f32 v49, v50, v51
	v_cvt_pk_bf16_f32 v52, v52, v53
	v_cvt_pk_bf16_f32 v53, v54, v55
	ds_write2st64_b64 v3, v[48:49], v[52:53] offset0:80 offset1:88
	s_waitcnt vmcnt(14)
	v_cvt_pk_bf16_f32 v56, v56, v57
	v_cvt_pk_bf16_f32 v57, v58, v59
	v_cvt_pk_bf16_f32 v60, v60, v61
	v_cvt_pk_bf16_f32 v61, v62, v63
	ds_write2st64_b64 v3, v[56:57], v[60:61] offset0:96 offset1:104
	s_waitcnt vmcnt(12)
	v_cvt_pk_bf16_f32 v64, v64, v65
	v_cvt_pk_bf16_f32 v65, v66, v67
	v_cvt_pk_bf16_f32 v68, v68, v69
	v_cvt_pk_bf16_f32 v69, v70, v71
	ds_write2st64_b64 v3, v[64:65], v[68:69] offset0:112 offset1:120
	s_waitcnt lgkmcnt(0)
	s_barrier
	v_mfma_f32_16x16x32_bf16 v[120:123], v[72:75], v[88:91], v[120:123]
	s_min_u32 s40, s25, 31
	s_bitcmp1_b32 s40, 4
	s_cselect_b32 s41, s23, s22
	s_lshl_b32 s42, s40, 23
	s_and_b32 s42, s42, 0x7000000
	s_or_b32 s41, s41, s42
	s_lshl_b32 s42, s40, 8
	s_and_b32 s42, s42, 0x100
	s_or_b32 s41, s41, s42
	s_sub_u32 s43, s25, 1
	s_min_u32 s43, s43, 31
	s_and_b32 s43, s43, 15
	s_lshl_b32 s43, s43, 15
	s_add_u32 s44, s43, s24
	v_mfma_f32_16x16x32_bf16 v[124:127], v[76:79], v[88:91], v[124:127]
	v_mfma_f32_16x16x32_bf16 v[128:131], v[80:83], v[88:91], v[128:131]
	v_mfma_f32_16x16x32_bf16 v[132:135], v[84:87], v[88:91], v[132:135]
	buffer_load_dwordx4 v[40:43], v1, s[4:7], s41 offen sc0 nt
	v_mfma_f32_16x16x32_bf16 v[136:139], v[72:75], v[92:95], v[136:139]
	v_mfma_f32_16x16x32_bf16 v[140:143], v[76:79], v[92:95], v[140:143]
	v_mfma_f32_16x16x32_bf16 v[144:147], v[80:83], v[92:95], v[144:147]
	v_mfma_f32_16x16x32_bf16 v[148:151], v[84:87], v[92:95], v[148:151]
	v_mfma_f32_16x16x32_bf16 v[152:155], v[72:75], v[96:99], v[152:155]
	v_mfma_f32_16x16x32_bf16 v[156:159], v[76:79], v[96:99], v[156:159]
	v_mfma_f32_16x16x32_bf16 v[160:163], v[80:83], v[96:99], v[160:163]
	v_mfma_f32_16x16x32_bf16 v[164:167], v[84:87], v[96:99], v[164:167]
	s_add_u32 s42, s41, 0x4000
	buffer_load_dwordx4 v[44:47], v1, s[4:7], s42 offen sc0 nt
	v_mfma_f32_16x16x32_bf16 v[168:171], v[72:75], v[100:103], v[168:171]
	v_mfma_f32_16x16x32_bf16 v[172:175], v[76:79], v[100:103], v[172:175]
	v_mfma_f32_16x16x32_bf16 v[176:179], v[80:83], v[100:103], v[176:179]
	v_mfma_f32_16x16x32_bf16 v[180:183], v[84:87], v[100:103], v[180:183]
	v_mfma_f32_16x16x32_bf16 v[184:187], v[72:75], v[104:107], v[184:187]
	v_mfma_f32_16x16x32_bf16 v[188:191], v[76:79], v[104:107], v[188:191]
	v_mfma_f32_16x16x32_bf16 v[192:195], v[80:83], v[104:107], v[192:195]
	v_mfma_f32_16x16x32_bf16 v[196:199], v[84:87], v[104:107], v[196:199]
	s_add_u32 s42, s41, 0x8000
	buffer_load_dwordx4 v[48:51], v1, s[4:7], s42 offen sc0 nt
	v_mfma_f32_16x16x32_bf16 v[200:203], v[72:75], v[108:111], v[200:203]
	v_mfma_f32_16x16x32_bf16 v[204:207], v[76:79], v[108:111], v[204:207]
	v_mfma_f32_16x16x32_bf16 v[208:211], v[80:83], v[108:111], v[208:211]
	v_mfma_f32_16x16x32_bf16 v[212:215], v[84:87], v[108:111], v[212:215]
	v_mfma_f32_16x16x32_bf16 v[216:219], v[72:75], v[112:115], v[216:219]
	v_mfma_f32_16x16x32_bf16 v[220:223], v[76:79], v[112:115], v[220:223]
	v_mfma_f32_16x16x32_bf16 v[224:227], v[80:83], v[112:115], v[224:227]
	v_mfma_f32_16x16x32_bf16 v[228:231], v[84:87], v[112:115], v[228:231]
	s_add_u32 s42, s41, 0xc000
	buffer_load_dwordx4 v[52:55], v1, s[4:7], s42 offen sc0 nt
	v_mfma_f32_16x16x32_bf16 v[232:235], v[72:75], v[116:119], v[232:235]
	v_mfma_f32_16x16x32_bf16 v[236:239], v[76:79], v[116:119], v[236:239]
	v_mfma_f32_16x16x32_bf16 v[240:243], v[80:83], v[116:119], v[240:243]
	v_mfma_f32_16x16x32_bf16 v[244:247], v[84:87], v[116:119], v[244:247]
	s_barrier
	ds_read_b128 v[72:75], v6 offset:1024
	ds_read_b128 v[76:79], v6 offset:3072
	ds_read_b128 v[80:83], v6 offset:5120
	ds_read_b128 v[84:87], v6 offset:7168
	ds_read_b128 v[88:91], v4 offset:1024
	ds_read_b128 v[92:95], v4 offset:3072
	ds_read_b128 v[96:99], v4 offset:5120
	ds_read_b128 v[100:103], v4 offset:7168
	ds_read_b128 v[104:107], v4 offset:9216
	ds_read_b128 v[108:111], v4 offset:11264
	ds_read_b128 v[112:115], v4 offset:13312
	ds_read_b128 v[116:119], v4 offset:15360
	s_waitcnt vmcnt(12)
	s_waitcnt lgkmcnt(0)
	s_barrier
	v_mfma_f32_16x16x32_bf16 v[120:123], v[72:75], v[88:91], v[120:123]
	s_add_u32 s33, s33, 0x8000
	s_cmp_eq_u32 s33, 0x18000
	s_cselect_b32 s33, 0, s33
	s_add_u32 s25, s25, 1
	s_mov_b32 m0, s26
	v_mfma_f32_16x16x32_bf16 v[124:127], v[76:79], v[88:91], v[124:127]
	buffer_load_dwordx4 v2, s[12:15], s44 offen sc1 lds
	v_mfma_f32_16x16x32_bf16 v[128:131], v[80:83], v[88:91], v[128:131]
	v_mfma_f32_16x16x32_bf16 v[132:135], v[84:87], v[88:91], v[132:135]
	v_mfma_f32_16x16x32_bf16 v[136:139], v[72:75], v[92:95], v[136:139]
	v_mfma_f32_16x16x32_bf16 v[140:143], v[76:79], v[92:95], v[140:143]
	s_add_u32 s42, s41, 0x10000
	buffer_load_dwordx4 v[56:59], v1, s[4:7], s42 offen sc0 nt
	v_mfma_f32_16x16x32_bf16 v[144:147], v[80:83], v[92:95], v[144:147]
	v_mfma_f32_16x16x32_bf16 v[148:151], v[84:87], v[92:95], v[148:151]
	v_mfma_f32_16x16x32_bf16 v[152:155], v[72:75], v[96:99], v[152:155]
	v_mfma_f32_16x16x32_bf16 v[156:159], v[76:79], v[96:99], v[156:159]
	buffer_load_dwordx4 v2, s[12:15], s44 offen offset:1024 sc1 lds
	v_mfma_f32_16x16x32_bf16 v[160:163], v[80:83], v[96:99], v[160:163]
	v_mfma_f32_16x16x32_bf16 v[164:167], v[84:87], v[96:99], v[164:167]
	v_mfma_f32_16x16x32_bf16 v[168:171], v[72:75], v[100:103], v[168:171]
	v_mfma_f32_16x16x32_bf16 v[172:175], v[76:79], v[100:103], v[172:175]
	s_add_u32 s42, s41, 0x14000
	buffer_load_dwordx4 v[60:63], v1, s[4:7], s42 offen sc0 nt
	v_mfma_f32_16x16x32_bf16 v[176:179], v[80:83], v[100:103], v[176:179]
	v_mfma_f32_16x16x32_bf16 v[180:183], v[84:87], v[100:103], v[180:183]
	v_mfma_f32_16x16x32_bf16 v[184:187], v[72:75], v[104:107], v[184:187]
	v_mfma_f32_16x16x32_bf16 v[188:191], v[76:79], v[104:107], v[188:191]
	buffer_load_dwordx4 v2, s[12:15], s44 offen offset:2048 sc1 lds
	v_mfma_f32_16x16x32_bf16 v[192:195], v[80:83], v[104:107], v[192:195]
	v_mfma_f32_16x16x32_bf16 v[196:199], v[84:87], v[104:107], v[196:199]
	v_mfma_f32_16x16x32_bf16 v[200:203], v[72:75], v[108:111], v[200:203]
	v_mfma_f32_16x16x32_bf16 v[204:207], v[76:79], v[108:111], v[204:207]
	s_add_u32 s42, s41, 0x18000
	buffer_load_dwordx4 v[64:67], v1, s[4:7], s42 offen sc0 nt
	v_mfma_f32_16x16x32_bf16 v[208:211], v[80:83], v[108:111], v[208:211]
	v_mfma_f32_16x16x32_bf16 v[212:215], v[84:87], v[108:111], v[212:215]
	v_mfma_f32_16x16x32_bf16 v[216:219], v[72:75], v[112:115], v[216:219]
	v_mfma_f32_16x16x32_bf16 v[220:223], v[76:79], v[112:115], v[220:223]
	buffer_load_dwordx4 v2, s[12:15], s44 offen offset:3072 sc1 lds
	v_mfma_f32_16x16x32_bf16 v[224:227], v[80:83], v[112:115], v[224:227]
	v_mfma_f32_16x16x32_bf16 v[228:231], v[84:87], v[112:115], v[228:231]
	v_mfma_f32_16x16x32_bf16 v[232:235], v[72:75], v[116:119], v[232:235]
	v_mfma_f32_16x16x32_bf16 v[236:239], v[76:79], v[116:119], v[236:239]
	s_add_u32 s42, s41, 0x1c000
	buffer_load_dwordx4 v[68:71], v1, s[4:7], s42 offen sc0 nt
	v_mfma_f32_16x16x32_bf16 v[240:243], v[80:83], v[116:119], v[240:243]
	s_add_u32 s26, s26, 0x8000
	s_cmp_eq_u32 s26, s32
	s_cselect_b32 s26, s27, s26
	v_mfma_f32_16x16x32_bf16 v[244:247], v[84:87], v[116:119], v[244:247]
	s_barrier
	v_add_u32_e32 v6, s33, v5
	ds_read_b128 v[72:75], v6 offset:0
	ds_read_b128 v[76:79], v6 offset:2048
	ds_read_b128 v[80:83], v6 offset:4096
	ds_read_b128 v[84:87], v6 offset:6144
	ds_read_b128 v[88:91], v4 offset:32768
	ds_read_b128 v[92:95], v4 offset:34816
	ds_read_b128 v[96:99], v4 offset:36864
	ds_read_b128 v[100:103], v4 offset:38912
	ds_read_b128 v[104:107], v4 offset:40960
	ds_read_b128 v[108:111], v4 offset:43008
	ds_read_b128 v[112:115], v4 offset:45056
	ds_read_b128 v[116:119], v4 offset:47104
	s_waitcnt vmcnt(18)
	v_cvt_pk_bf16_f32 v8, v8, v9
	v_cvt_pk_bf16_f32 v9, v10, v11
	v_cvt_pk_bf16_f32 v12, v12, v13
	v_cvt_pk_bf16_f32 v13, v14, v15
	ds_write2st64_b64 v3, v[8:9], v[12:13] offset0:0 offset1:8
	s_waitcnt vmcnt(16)
	v_cvt_pk_bf16_f32 v16, v16, v17
	v_cvt_pk_bf16_f32 v17, v18, v19
	v_cvt_pk_bf16_f32 v20, v20, v21
	v_cvt_pk_bf16_f32 v21, v22, v23
	ds_write2st64_b64 v3, v[16:17], v[20:21] offset0:16 offset1:24
	s_waitcnt vmcnt(14)
	v_cvt_pk_bf16_f32 v24, v24, v25
	v_cvt_pk_bf16_f32 v25, v26, v27
	v_cvt_pk_bf16_f32 v28, v28, v29
	v_cvt_pk_bf16_f32 v29, v30, v31
	ds_write2st64_b64 v3, v[24:25], v[28:29] offset0:32 offset1:40
	s_waitcnt vmcnt(12)
	v_cvt_pk_bf16_f32 v32, v32, v33
	v_cvt_pk_bf16_f32 v33, v34, v35
	v_cvt_pk_bf16_f32 v36, v36, v37
	v_cvt_pk_bf16_f32 v37, v38, v39
	ds_write2st64_b64 v3, v[32:33], v[36:37] offset0:48 offset1:56
	s_waitcnt lgkmcnt(0)
	s_barrier
	v_mfma_f32_16x16x32_bf16 v[120:123], v[72:75], v[88:91], v[120:123]
	s_min_u32 s40, s25, 31
	s_bitcmp1_b32 s40, 4
	s_cselect_b32 s41, s23, s22
	s_lshl_b32 s42, s40, 23
	s_and_b32 s42, s42, 0x7000000
	s_or_b32 s41, s41, s42
	s_lshl_b32 s42, s40, 8
	s_and_b32 s42, s42, 0x100
	s_or_b32 s41, s41, s42
	s_sub_u32 s43, s25, 1
	s_min_u32 s43, s43, 31
	s_and_b32 s43, s43, 15
	s_lshl_b32 s43, s43, 15
	s_add_u32 s44, s43, s24
	v_mfma_f32_16x16x32_bf16 v[124:127], v[76:79], v[88:91], v[124:127]
	v_mfma_f32_16x16x32_bf16 v[128:131], v[80:83], v[88:91], v[128:131]
	v_mfma_f32_16x16x32_bf16 v[132:135], v[84:87], v[88:91], v[132:135]
	buffer_load_dwordx4 v[8:11], v1, s[4:7], s41 offen sc0 nt
	v_mfma_f32_16x16x32_bf16 v[136:139], v[72:75], v[92:95], v[136:139]
	v_mfma_f32_16x16x32_bf16 v[140:143], v[76:79], v[92:95], v[140:143]
	v_mfma_f32_16x16x32_bf16 v[144:147], v[80:83], v[92:95], v[144:147]
	v_mfma_f32_16x16x32_bf16 v[148:151], v[84:87], v[92:95], v[148:151]
	v_mfma_f32_16x16x32_bf16 v[152:155], v[72:75], v[96:99], v[152:155]
	v_mfma_f32_16x16x32_bf16 v[156:159], v[76:79], v[96:99], v[156:159]
	v_mfma_f32_16x16x32_bf16 v[160:163], v[80:83], v[96:99], v[160:163]
	v_mfma_f32_16x16x32_bf16 v[164:167], v[84:87], v[96:99], v[164:167]
	s_add_u32 s42, s41, 0x4000
	buffer_load_dwordx4 v[12:15], v1, s[4:7], s42 offen sc0 nt
	v_mfma_f32_16x16x32_bf16 v[168:171], v[72:75], v[100:103], v[168:171]
	v_mfma_f32_16x16x32_bf16 v[172:175], v[76:79], v[100:103], v[172:175]
	v_mfma_f32_16x16x32_bf16 v[176:179], v[80:83], v[100:103], v[176:179]
	v_mfma_f32_16x16x32_bf16 v[180:183], v[84:87], v[100:103], v[180:183]
	v_mfma_f32_16x16x32_bf16 v[184:187], v[72:75], v[104:107], v[184:187]
	v_mfma_f32_16x16x32_bf16 v[188:191], v[76:79], v[104:107], v[188:191]
	v_mfma_f32_16x16x32_bf16 v[192:195], v[80:83], v[104:107], v[192:195]
	v_mfma_f32_16x16x32_bf16 v[196:199], v[84:87], v[104:107], v[196:199]
	s_add_u32 s42, s41, 0x8000
	buffer_load_dwordx4 v[16:19], v1, s[4:7], s42 offen sc0 nt
	v_mfma_f32_16x16x32_bf16 v[200:203], v[72:75], v[108:111], v[200:203]
	v_mfma_f32_16x16x32_bf16 v[204:207], v[76:79], v[108:111], v[204:207]
	v_mfma_f32_16x16x32_bf16 v[208:211], v[80:83], v[108:111], v[208:211]
	v_mfma_f32_16x16x32_bf16 v[212:215], v[84:87], v[108:111], v[212:215]
	v_mfma_f32_16x16x32_bf16 v[216:219], v[72:75], v[112:115], v[216:219]
	v_mfma_f32_16x16x32_bf16 v[220:223], v[76:79], v[112:115], v[220:223]
	v_mfma_f32_16x16x32_bf16 v[224:227], v[80:83], v[112:115], v[224:227]
	v_mfma_f32_16x16x32_bf16 v[228:231], v[84:87], v[112:115], v[228:231]
	s_add_u32 s42, s41, 0xc000
	buffer_load_dwordx4 v[20:23], v1, s[4:7], s42 offen sc0 nt
	v_mfma_f32_16x16x32_bf16 v[232:235], v[72:75], v[116:119], v[232:235]
	v_mfma_f32_16x16x32_bf16 v[236:239], v[76:79], v[116:119], v[236:239]
	v_mfma_f32_16x16x32_bf16 v[240:243], v[80:83], v[116:119], v[240:243]
	v_mfma_f32_16x16x32_bf16 v[244:247], v[84:87], v[116:119], v[244:247]
	s_barrier
	ds_read_b128 v[72:75], v6 offset:1024
	ds_read_b128 v[76:79], v6 offset:3072
	ds_read_b128 v[80:83], v6 offset:5120
	ds_read_b128 v[84:87], v6 offset:7168
	ds_read_b128 v[88:91], v4 offset:33792
	ds_read_b128 v[92:95], v4 offset:35840
	ds_read_b128 v[96:99], v4 offset:37888
	ds_read_b128 v[100:103], v4 offset:39936
	ds_read_b128 v[104:107], v4 offset:41984
	ds_read_b128 v[108:111], v4 offset:44032
	ds_read_b128 v[112:115], v4 offset:46080
	ds_read_b128 v[116:119], v4 offset:48128
	s_waitcnt vmcnt(5)
	s_waitcnt lgkmcnt(0)
	s_barrier
	v_mfma_f32_16x16x32_bf16 v[120:123], v[72:75], v[88:91], v[120:123]
	s_add_u32 s33, s33, 0x8000
	s_cmp_eq_u32 s33, 0x18000
	s_cselect_b32 s33, 0, s33
	s_add_u32 s25, s25, 1
	s_mov_b32 m0, s26
	v_mfma_f32_16x16x32_bf16 v[124:127], v[76:79], v[88:91], v[124:127]
	buffer_load_dwordx4 v2, s[12:15], s44 offen sc1 lds
	v_mfma_f32_16x16x32_bf16 v[128:131], v[80:83], v[88:91], v[128:131]
	v_mfma_f32_16x16x32_bf16 v[132:135], v[84:87], v[88:91], v[132:135]
	v_mfma_f32_16x16x32_bf16 v[136:139], v[72:75], v[92:95], v[136:139]
	v_mfma_f32_16x16x32_bf16 v[140:143], v[76:79], v[92:95], v[140:143]
	s_add_u32 s42, s41, 0x10000
	buffer_load_dwordx4 v[24:27], v1, s[4:7], s42 offen sc0 nt
	v_mfma_f32_16x16x32_bf16 v[144:147], v[80:83], v[92:95], v[144:147]
	v_mfma_f32_16x16x32_bf16 v[148:151], v[84:87], v[92:95], v[148:151]
	v_mfma_f32_16x16x32_bf16 v[152:155], v[72:75], v[96:99], v[152:155]
	v_mfma_f32_16x16x32_bf16 v[156:159], v[76:79], v[96:99], v[156:159]
	buffer_load_dwordx4 v2, s[12:15], s44 offen offset:1024 sc1 lds
	v_mfma_f32_16x16x32_bf16 v[160:163], v[80:83], v[96:99], v[160:163]
	v_mfma_f32_16x16x32_bf16 v[164:167], v[84:87], v[96:99], v[164:167]
	v_mfma_f32_16x16x32_bf16 v[168:171], v[72:75], v[100:103], v[168:171]
	v_mfma_f32_16x16x32_bf16 v[172:175], v[76:79], v[100:103], v[172:175]
	s_add_u32 s42, s41, 0x14000
	buffer_load_dwordx4 v[28:31], v1, s[4:7], s42 offen sc0 nt
	v_mfma_f32_16x16x32_bf16 v[176:179], v[80:83], v[100:103], v[176:179]
	v_mfma_f32_16x16x32_bf16 v[180:183], v[84:87], v[100:103], v[180:183]
	v_mfma_f32_16x16x32_bf16 v[184:187], v[72:75], v[104:107], v[184:187]
	v_mfma_f32_16x16x32_bf16 v[188:191], v[76:79], v[104:107], v[188:191]
	buffer_load_dwordx4 v2, s[12:15], s44 offen offset:2048 sc1 lds
	v_mfma_f32_16x16x32_bf16 v[192:195], v[80:83], v[104:107], v[192:195]
	v_mfma_f32_16x16x32_bf16 v[196:199], v[84:87], v[104:107], v[196:199]
	v_mfma_f32_16x16x32_bf16 v[200:203], v[72:75], v[108:111], v[200:203]
	v_mfma_f32_16x16x32_bf16 v[204:207], v[76:79], v[108:111], v[204:207]
	s_add_u32 s42, s41, 0x18000
	buffer_load_dwordx4 v[32:35], v1, s[4:7], s42 offen sc0 nt
	v_mfma_f32_16x16x32_bf16 v[208:211], v[80:83], v[108:111], v[208:211]
	v_mfma_f32_16x16x32_bf16 v[212:215], v[84:87], v[108:111], v[212:215]
	v_mfma_f32_16x16x32_bf16 v[216:219], v[72:75], v[112:115], v[216:219]
	v_mfma_f32_16x16x32_bf16 v[220:223], v[76:79], v[112:115], v[220:223]
	buffer_load_dwordx4 v2, s[12:15], s44 offen offset:3072 sc1 lds
	v_mfma_f32_16x16x32_bf16 v[224:227], v[80:83], v[112:115], v[224:227]
	v_mfma_f32_16x16x32_bf16 v[228:231], v[84:87], v[112:115], v[228:231]
	v_mfma_f32_16x16x32_bf16 v[232:235], v[72:75], v[116:119], v[232:235]
	v_mfma_f32_16x16x32_bf16 v[236:239], v[76:79], v[116:119], v[236:239]
	s_add_u32 s42, s41, 0x1c000
	buffer_load_dwordx4 v[36:39], v1, s[4:7], s42 offen sc0 nt
	v_mfma_f32_16x16x32_bf16 v[240:243], v[80:83], v[116:119], v[240:243]
	s_add_u32 s26, s26, 0x8000
	s_cmp_eq_u32 s26, s32
	s_cselect_b32 s26, s27, s26
	v_mfma_f32_16x16x32_bf16 v[244:247], v[84:87], v[116:119], v[244:247]
	s_barrier
	s_mov_b32 s38, 7
.Lg_loop0:
	v_add_u32_e32 v6, s33, v5
	ds_read_b128 v[72:75], v6 offset:0
	ds_read_b128 v[76:79], v6 offset:2048
	ds_read_b128 v[80:83], v6 offset:4096
	ds_read_b128 v[84:87], v6 offset:6144
	ds_read_b128 v[88:91], v4 offset:0
	ds_read_b128 v[92:95], v4 offset:2048
	ds_read_b128 v[96:99], v4 offset:4096
	ds_read_b128 v[100:103], v4 offset:6144
	ds_read_b128 v[104:107], v4 offset:8192
	ds_read_b128 v[108:111], v4 offset:10240
	ds_read_b128 v[112:115], v4 offset:12288
	ds_read_b128 v[116:119], v4 offset:14336
	s_waitcnt vmcnt(22)
	v_cvt_pk_bf16_f32 v40, v40, v41
	v_cvt_pk_bf16_f32 v41, v42, v43
	v_cvt_pk_bf16_f32 v44, v44, v45
	v_cvt_pk_bf16_f32 v45, v46, v47
	ds_write2st64_b64 v3, v[40:41], v[44:45] offset0:64 offset1:72
	s_waitcnt vmcnt(20)
	v_cvt_pk_bf16_f32 v48, v48, v49
	v_cvt_pk_bf16_f32 v49, v50, v51
	v_cvt_pk_bf16_f32 v52, v52, v53
	v_cvt_pk_bf16_f32 v53, v54, v55
	ds_write2st64_b64 v3, v[48:49], v[52:53] offset0:80 offset1:88
	s_waitcnt vmcnt(16)
	v_cvt_pk_bf16_f32 v56, v56, v57
	v_cvt_pk_bf16_f32 v57, v58, v59
	v_cvt_pk_bf16_f32 v60, v60, v61
	v_cvt_pk_bf16_f32 v61, v62, v63
	ds_write2st64_b64 v3, v[56:57], v[60:61] offset0:96 offset1:104
	s_waitcnt vmcnt(12)
	v_cvt_pk_bf16_f32 v64, v64, v65
	v_cvt_pk_bf16_f32 v65, v66, v67
	v_cvt_pk_bf16_f32 v68, v68, v69
	v_cvt_pk_bf16_f32 v69, v70, v71
	ds_write2st64_b64 v3, v[64:65], v[68:69] offset0:112 offset1:120
	s_waitcnt lgkmcnt(0)
	s_barrier
	v_mfma_f32_16x16x32_bf16 v[120:123], v[72:75], v[88:91], v[120:123]
	s_min_u32 s40, s25, 31
	s_bitcmp1_b32 s40, 4
	s_cselect_b32 s41, s23, s22
	s_lshl_b32 s42, s40, 23
	s_and_b32 s42, s42, 0x7000000
	s_or_b32 s41, s41, s42
	s_lshl_b32 s42, s40, 8
	s_and_b32 s42, s42, 0x100
	s_or_b32 s41, s41, s42
	s_sub_u32 s43, s25, 1
	s_min_u32 s43, s43, 31
	s_and_b32 s43, s43, 15
	s_lshl_b32 s43, s43, 15
	s_add_u32 s44, s43, s24
	v_mfma_f32_16x16x32_bf16 v[124:127], v[76:79], v[88:91], v[124:127]
	v_mfma_f32_16x16x32_bf16 v[128:131], v[80:83], v[88:91], v[128:131]
	v_mfma_f32_16x16x32_bf16 v[132:135], v[84:87], v[88:91], v[132:135]
	buffer_load_dwordx4 v[40:43], v1, s[4:7], s41 offen sc0 nt
	v_mfma_f32_16x16x32_bf16 v[136:139], v[72:75], v[92:95], v[136:139]
	v_mfma_f32_16x16x32_bf16 v[140:143], v[76:79], v[92:95], v[140:143]
	v_mfma_f32_16x16x32_bf16 v[144:147], v[80:83], v[92:95], v[144:147]
	v_mfma_f32_16x16x32_bf16 v[148:151], v[84:87], v[92:95], v[148:151]
	v_mfma_f32_16x16x32_bf16 v[152:155], v[72:75], v[96:99], v[152:155]
	v_mfma_f32_16x16x32_bf16 v[156:159], v[76:79], v[96:99], v[156:159]
	v_mfma_f32_16x16x32_bf16 v[160:163], v[80:83], v[96:99], v[160:163]
	v_mfma_f32_16x16x32_bf16 v[164:167], v[84:87], v[96:99], v[164:167]
	s_add_u32 s42, s41, 0x4000
	buffer_load_dwordx4 v[44:47], v1, s[4:7], s42 offen sc0 nt
	v_mfma_f32_16x16x32_bf16 v[168:171], v[72:75], v[100:103], v[168:171]
	v_mfma_f32_16x16x32_bf16 v[172:175], v[76:79], v[100:103], v[172:175]
	v_mfma_f32_16x16x32_bf16 v[176:179], v[80:83], v[100:103], v[176:179]
	v_mfma_f32_16x16x32_bf16 v[180:183], v[84:87], v[100:103], v[180:183]
	v_mfma_f32_16x16x32_bf16 v[184:187], v[72:75], v[104:107], v[184:187]
	v_mfma_f32_16x16x32_bf16 v[188:191], v[76:79], v[104:107], v[188:191]
	v_mfma_f32_16x16x32_bf16 v[192:195], v[80:83], v[104:107], v[192:195]
	v_mfma_f32_16x16x32_bf16 v[196:199], v[84:87], v[104:107], v[196:199]
	s_add_u32 s42, s41, 0x8000
	buffer_load_dwordx4 v[48:51], v1, s[4:7], s42 offen sc0 nt
	v_mfma_f32_16x16x32_bf16 v[200:203], v[72:75], v[108:111], v[200:203]
	v_mfma_f32_16x16x32_bf16 v[204:207], v[76:79], v[108:111], v[204:207]
	v_mfma_f32_16x16x32_bf16 v[208:211], v[80:83], v[108:111], v[208:211]
	v_mfma_f32_16x16x32_bf16 v[212:215], v[84:87], v[108:111], v[212:215]
	v_mfma_f32_16x16x32_bf16 v[216:219], v[72:75], v[112:115], v[216:219]
	v_mfma_f32_16x16x32_bf16 v[220:223], v[76:79], v[112:115], v[220:223]
	v_mfma_f32_16x16x32_bf16 v[224:227], v[80:83], v[112:115], v[224:227]
	v_mfma_f32_16x16x32_bf16 v[228:231], v[84:87], v[112:115], v[228:231]
	s_add_u32 s42, s41, 0xc000
	buffer_load_dwordx4 v[52:55], v1, s[4:7], s42 offen sc0 nt
	v_mfma_f32_16x16x32_bf16 v[232:235], v[72:75], v[116:119], v[232:235]
	v_mfma_f32_16x16x32_bf16 v[236:239], v[76:79], v[116:119], v[236:239]
	v_mfma_f32_16x16x32_bf16 v[240:243], v[80:83], v[116:119], v[240:243]
	v_mfma_f32_16x16x32_bf16 v[244:247], v[84:87], v[116:119], v[244:247]
	s_barrier
	ds_read_b128 v[72:75], v6 offset:1024
	ds_read_b128 v[76:79], v6 offset:3072
	ds_read_b128 v[80:83], v6 offset:5120
	ds_read_b128 v[84:87], v6 offset:7168
	ds_read_b128 v[88:91], v4 offset:1024
	ds_read_b128 v[92:95], v4 offset:3072
	ds_read_b128 v[96:99], v4 offset:5120
	ds_read_b128 v[100:103], v4 offset:7168
	ds_read_b128 v[104:107], v4 offset:9216
	ds_read_b128 v[108:111], v4 offset:11264
	ds_read_b128 v[112:115], v4 offset:13312
	ds_read_b128 v[116:119], v4 offset:15360
	s_waitcnt vmcnt(5)
	s_waitcnt lgkmcnt(0)
	s_barrier
	v_mfma_f32_16x16x32_bf16 v[120:123], v[72:75], v[88:91], v[120:123]
	s_add_u32 s33, s33, 0x8000
	s_cmp_eq_u32 s33, 0x18000
	s_cselect_b32 s33, 0, s33
	s_add_u32 s25, s25, 1
	s_mov_b32 m0, s26
	v_mfma_f32_16x16x32_bf16 v[124:127], v[76:79], v[88:91], v[124:127]
	buffer_load_dwordx4 v2, s[12:15], s44 offen sc1 lds
	v_mfma_f32_16x16x32_bf16 v[128:131], v[80:83], v[88:91], v[128:131]
	v_mfma_f32_16x16x32_bf16 v[132:135], v[84:87], v[88:91], v[132:135]
	v_mfma_f32_16x16x32_bf16 v[136:139], v[72:75], v[92:95], v[136:139]
	v_mfma_f32_16x16x32_bf16 v[140:143], v[76:79], v[92:95], v[140:143]
	s_add_u32 s42, s41, 0x10000
	buffer_load_dwordx4 v[56:59], v1, s[4:7], s42 offen sc0 nt
	v_mfma_f32_16x16x32_bf16 v[144:147], v[80:83], v[92:95], v[144:147]
	v_mfma_f32_16x16x32_bf16 v[148:151], v[84:87], v[92:95], v[148:151]
	v_mfma_f32_16x16x32_bf16 v[152:155], v[72:75], v[96:99], v[152:155]
	v_mfma_f32_16x16x32_bf16 v[156:159], v[76:79], v[96:99], v[156:159]
	buffer_load_dwordx4 v2, s[12:15], s44 offen offset:1024 sc1 lds
	v_mfma_f32_16x16x32_bf16 v[160:163], v[80:83], v[96:99], v[160:163]
	v_mfma_f32_16x16x32_bf16 v[164:167], v[84:87], v[96:99], v[164:167]
	v_mfma_f32_16x16x32_bf16 v[168:171], v[72:75], v[100:103], v[168:171]
	v_mfma_f32_16x16x32_bf16 v[172:175], v[76:79], v[100:103], v[172:175]
	s_add_u32 s42, s41, 0x14000
	buffer_load_dwordx4 v[60:63], v1, s[4:7], s42 offen sc0 nt
	v_mfma_f32_16x16x32_bf16 v[176:179], v[80:83], v[100:103], v[176:179]
	v_mfma_f32_16x16x32_bf16 v[180:183], v[84:87], v[100:103], v[180:183]
	v_mfma_f32_16x16x32_bf16 v[184:187], v[72:75], v[104:107], v[184:187]
	v_mfma_f32_16x16x32_bf16 v[188:191], v[76:79], v[104:107], v[188:191]
	buffer_load_dwordx4 v2, s[12:15], s44 offen offset:2048 sc1 lds
	v_mfma_f32_16x16x32_bf16 v[192:195], v[80:83], v[104:107], v[192:195]
	v_mfma_f32_16x16x32_bf16 v[196:199], v[84:87], v[104:107], v[196:199]
	v_mfma_f32_16x16x32_bf16 v[200:203], v[72:75], v[108:111], v[200:203]
	v_mfma_f32_16x16x32_bf16 v[204:207], v[76:79], v[108:111], v[204:207]
	s_add_u32 s42, s41, 0x18000
	buffer_load_dwordx4 v[64:67], v1, s[4:7], s42 offen sc0 nt
	v_mfma_f32_16x16x32_bf16 v[208:211], v[80:83], v[108:111], v[208:211]
	v_mfma_f32_16x16x32_bf16 v[212:215], v[84:87], v[108:111], v[212:215]
	v_mfma_f32_16x16x32_bf16 v[216:219], v[72:75], v[112:115], v[216:219]
	v_mfma_f32_16x16x32_bf16 v[220:223], v[76:79], v[112:115], v[220:223]
	buffer_load_dwordx4 v2, s[12:15], s44 offen offset:3072 sc1 lds
	v_mfma_f32_16x16x32_bf16 v[224:227], v[80:83], v[112:115], v[224:227]
	v_mfma_f32_16x16x32_bf16 v[228:231], v[84:87], v[112:115], v[228:231]
	v_mfma_f32_16x16x32_bf16 v[232:235], v[72:75], v[116:119], v[232:235]
	v_mfma_f32_16x16x32_bf16 v[236:239], v[76:79], v[116:119], v[236:239]
	s_add_u32 s42, s41, 0x1c000
	buffer_load_dwordx4 v[68:71], v1, s[4:7], s42 offen sc0 nt
	v_mfma_f32_16x16x32_bf16 v[240:243], v[80:83], v[116:119], v[240:243]
	s_add_u32 s26, s26, 0x8000
	s_cmp_eq_u32 s26, s32
	s_cselect_b32 s26, s27, s26
	v_mfma_f32_16x16x32_bf16 v[244:247], v[84:87], v[116:119], v[244:247]
	s_barrier
	v_add_u32_e32 v6, s33, v5
	ds_read_b128 v[72:75], v6 offset:0
	ds_read_b128 v[76:79], v6 offset:2048
	ds_read_b128 v[80:83], v6 offset:4096
	ds_read_b128 v[84:87], v6 offset:6144
	ds_read_b128 v[88:91], v4 offset:32768
	ds_read_b128 v[92:95], v4 offset:34816
	ds_read_b128 v[96:99], v4 offset:36864
	ds_read_b128 v[100:103], v4 offset:38912
	ds_read_b128 v[104:107], v4 offset:40960
	ds_read_b128 v[108:111], v4 offset:43008
	ds_read_b128 v[112:115], v4 offset:45056
	ds_read_b128 v[116:119], v4 offset:47104
	s_waitcnt vmcnt(22)
	v_cvt_pk_bf16_f32 v8, v8, v9
	v_cvt_pk_bf16_f32 v9, v10, v11
	v_cvt_pk_bf16_f32 v12, v12, v13
	v_cvt_pk_bf16_f32 v13, v14, v15
	ds_write2st64_b64 v3, v[8:9], v[12:13] offset0:0 offset1:8
	s_waitcnt vmcnt(20)
	v_cvt_pk_bf16_f32 v16, v16, v17
	v_cvt_pk_bf16_f32 v17, v18, v19
	v_cvt_pk_bf16_f32 v20, v20, v21
	v_cvt_pk_bf16_f32 v21, v22, v23
	ds_write2st64_b64 v3, v[16:17], v[20:21] offset0:16 offset1:24
	s_waitcnt vmcnt(16)
	v_cvt_pk_bf16_f32 v24, v24, v25
	v_cvt_pk_bf16_f32 v25, v26, v27
	v_cvt_pk_bf16_f32 v28, v28, v29
	v_cvt_pk_bf16_f32 v29, v30, v31
	ds_write2st64_b64 v3, v[24:25], v[28:29] offset0:32 offset1:40
	s_waitcnt vmcnt(12)
	v_cvt_pk_bf16_f32 v32, v32, v33
	v_cvt_pk_bf16_f32 v33, v34, v35
	v_cvt_pk_bf16_f32 v36, v36, v37
	v_cvt_pk_bf16_f32 v37, v38, v39
	ds_write2st64_b64 v3, v[32:33], v[36:37] offset0:48 offset1:56
	s_waitcnt lgkmcnt(0)
	s_barrier
	v_mfma_f32_16x16x32_bf16 v[120:123], v[72:75], v[88:91], v[120:123]
	s_min_u32 s40, s25, 31
	s_bitcmp1_b32 s40, 4
	s_cselect_b32 s41, s23, s22
	s_lshl_b32 s42, s40, 23
	s_and_b32 s42, s42, 0x7000000
	s_or_b32 s41, s41, s42
	s_lshl_b32 s42, s40, 8
	s_and_b32 s42, s42, 0x100
	s_or_b32 s41, s41, s42
	s_sub_u32 s43, s25, 1
	s_min_u32 s43, s43, 31
	s_and_b32 s43, s43, 15
	s_lshl_b32 s43, s43, 15
	s_add_u32 s44, s43, s24
	v_mfma_f32_16x16x32_bf16 v[124:127], v[76:79], v[88:91], v[124:127]
	v_mfma_f32_16x16x32_bf16 v[128:131], v[80:83], v[88:91], v[128:131]
	v_mfma_f32_16x16x32_bf16 v[132:135], v[84:87], v[88:91], v[132:135]
	buffer_load_dwordx4 v[8:11], v1, s[4:7], s41 offen sc0 nt
	v_mfma_f32_16x16x32_bf16 v[136:139], v[72:75], v[92:95], v[136:139]
	v_mfma_f32_16x16x32_bf16 v[140:143], v[76:79], v[92:95], v[140:143]
	v_mfma_f32_16x16x32_bf16 v[144:147], v[80:83], v[92:95], v[144:147]
	v_mfma_f32_16x16x32_bf16 v[148:151], v[84:87], v[92:95], v[148:151]
	v_mfma_f32_16x16x32_bf16 v[152:155], v[72:75], v[96:99], v[152:155]
	v_mfma_f32_16x16x32_bf16 v[156:159], v[76:79], v[96:99], v[156:159]
	v_mfma_f32_16x16x32_bf16 v[160:163], v[80:83], v[96:99], v[160:163]
	v_mfma_f32_16x16x32_bf16 v[164:167], v[84:87], v[96:99], v[164:167]
	s_add_u32 s42, s41, 0x4000
	buffer_load_dwordx4 v[12:15], v1, s[4:7], s42 offen sc0 nt
	v_mfma_f32_16x16x32_bf16 v[168:171], v[72:75], v[100:103], v[168:171]
	v_mfma_f32_16x16x32_bf16 v[172:175], v[76:79], v[100:103], v[172:175]
	v_mfma_f32_16x16x32_bf16 v[176:179], v[80:83], v[100:103], v[176:179]
	v_mfma_f32_16x16x32_bf16 v[180:183], v[84:87], v[100:103], v[180:183]
	v_mfma_f32_16x16x32_bf16 v[184:187], v[72:75], v[104:107], v[184:187]
	v_mfma_f32_16x16x32_bf16 v[188:191], v[76:79], v[104:107], v[188:191]
	v_mfma_f32_16x16x32_bf16 v[192:195], v[80:83], v[104:107], v[192:195]
	v_mfma_f32_16x16x32_bf16 v[196:199], v[84:87], v[104:107], v[196:199]
	s_add_u32 s42, s41, 0x8000
	buffer_load_dwordx4 v[16:19], v1, s[4:7], s42 offen sc0 nt
	v_mfma_f32_16x16x32_bf16 v[200:203], v[72:75], v[108:111], v[200:203]
	v_mfma_f32_16x16x32_bf16 v[204:207], v[76:79], v[108:111], v[204:207]
	v_mfma_f32_16x16x32_bf16 v[208:211], v[80:83], v[108:111], v[208:211]
	v_mfma_f32_16x16x32_bf16 v[212:215], v[84:87], v[108:111], v[212:215]
	v_mfma_f32_16x16x32_bf16 v[216:219], v[72:75], v[112:115], v[216:219]
	v_mfma_f32_16x16x32_bf16 v[220:223], v[76:79], v[112:115], v[220:223]
	v_mfma_f32_16x16x32_bf16 v[224:227], v[80:83], v[112:115], v[224:227]
	v_mfma_f32_16x16x32_bf16 v[228:231], v[84:87], v[112:115], v[228:231]
	s_add_u32 s42, s41, 0xc000
	buffer_load_dwordx4 v[20:23], v1, s[4:7], s42 offen sc0 nt
	v_mfma_f32_16x16x32_bf16 v[232:235], v[72:75], v[116:119], v[232:235]
	v_mfma_f32_16x16x32_bf16 v[236:239], v[76:79], v[116:119], v[236:239]
	v_mfma_f32_16x16x32_bf16 v[240:243], v[80:83], v[116:119], v[240:243]
	v_mfma_f32_16x16x32_bf16 v[244:247], v[84:87], v[116:119], v[244:247]
	s_barrier
	ds_read_b128 v[72:75], v6 offset:1024
	ds_read_b128 v[76:79], v6 offset:3072
	ds_read_b128 v[80:83], v6 offset:5120
	ds_read_b128 v[84:87], v6 offset:7168
	ds_read_b128 v[88:91], v4 offset:33792
	ds_read_b128 v[92:95], v4 offset:35840
	ds_read_b128 v[96:99], v4 offset:37888
	ds_read_b128 v[100:103], v4 offset:39936
	ds_read_b128 v[104:107], v4 offset:41984
	ds_read_b128 v[108:111], v4 offset:44032
	ds_read_b128 v[112:115], v4 offset:46080
	ds_read_b128 v[116:119], v4 offset:48128
	s_waitcnt vmcnt(5)
	s_waitcnt lgkmcnt(0)
	s_barrier
	v_mfma_f32_16x16x32_bf16 v[120:123], v[72:75], v[88:91], v[120:123]
	s_add_u32 s33, s33, 0x8000
	s_cmp_eq_u32 s33, 0x18000
	s_cselect_b32 s33, 0, s33
	s_add_u32 s25, s25, 1
	s_mov_b32 m0, s26
	v_mfma_f32_16x16x32_bf16 v[124:127], v[76:79], v[88:91], v[124:127]
	buffer_load_dwordx4 v2, s[12:15], s44 offen sc1 lds
	v_mfma_f32_16x16x32_bf16 v[128:131], v[80:83], v[88:91], v[128:131]
	v_mfma_f32_16x16x32_bf16 v[132:135], v[84:87], v[88:91], v[132:135]
	v_mfma_f32_16x16x32_bf16 v[136:139], v[72:75], v[92:95], v[136:139]
	v_mfma_f32_16x16x32_bf16 v[140:143], v[76:79], v[92:95], v[140:143]
	s_add_u32 s42, s41, 0x10000
	buffer_load_dwordx4 v[24:27], v1, s[4:7], s42 offen sc0 nt
	v_mfma_f32_16x16x32_bf16 v[144:147], v[80:83], v[92:95], v[144:147]
	v_mfma_f32_16x16x32_bf16 v[148:151], v[84:87], v[92:95], v[148:151]
	v_mfma_f32_16x16x32_bf16 v[152:155], v[72:75], v[96:99], v[152:155]
	v_mfma_f32_16x16x32_bf16 v[156:159], v[76:79], v[96:99], v[156:159]
	buffer_load_dwordx4 v2, s[12:15], s44 offen offset:1024 sc1 lds
	v_mfma_f32_16x16x32_bf16 v[160:163], v[80:83], v[96:99], v[160:163]
	v_mfma_f32_16x16x32_bf16 v[164:167], v[84:87], v[96:99], v[164:167]
	v_mfma_f32_16x16x32_bf16 v[168:171], v[72:75], v[100:103], v[168:171]
	v_mfma_f32_16x16x32_bf16 v[172:175], v[76:79], v[100:103], v[172:175]
	s_add_u32 s42, s41, 0x14000
	buffer_load_dwordx4 v[28:31], v1, s[4:7], s42 offen sc0 nt
	v_mfma_f32_16x16x32_bf16 v[176:179], v[80:83], v[100:103], v[176:179]
	v_mfma_f32_16x16x32_bf16 v[180:183], v[84:87], v[100:103], v[180:183]
	v_mfma_f32_16x16x32_bf16 v[184:187], v[72:75], v[104:107], v[184:187]
	v_mfma_f32_16x16x32_bf16 v[188:191], v[76:79], v[104:107], v[188:191]
	buffer_load_dwordx4 v2, s[12:15], s44 offen offset:2048 sc1 lds
	v_mfma_f32_16x16x32_bf16 v[192:195], v[80:83], v[104:107], v[192:195]
	v_mfma_f32_16x16x32_bf16 v[196:199], v[84:87], v[104:107], v[196:199]
	v_mfma_f32_16x16x32_bf16 v[200:203], v[72:75], v[108:111], v[200:203]
	v_mfma_f32_16x16x32_bf16 v[204:207], v[76:79], v[108:111], v[204:207]
	s_add_u32 s42, s41, 0x18000
	buffer_load_dwordx4 v[32:35], v1, s[4:7], s42 offen sc0 nt
	v_mfma_f32_16x16x32_bf16 v[208:211], v[80:83], v[108:111], v[208:211]
	v_mfma_f32_16x16x32_bf16 v[212:215], v[84:87], v[108:111], v[212:215]
	v_mfma_f32_16x16x32_bf16 v[216:219], v[72:75], v[112:115], v[216:219]
	v_mfma_f32_16x16x32_bf16 v[220:223], v[76:79], v[112:115], v[220:223]
	buffer_load_dwordx4 v2, s[12:15], s44 offen offset:3072 sc1 lds
	v_mfma_f32_16x16x32_bf16 v[224:227], v[80:83], v[112:115], v[224:227]
	v_mfma_f32_16x16x32_bf16 v[228:231], v[84:87], v[112:115], v[228:231]
	v_mfma_f32_16x16x32_bf16 v[232:235], v[72:75], v[116:119], v[232:235]
	v_mfma_f32_16x16x32_bf16 v[236:239], v[76:79], v[116:119], v[236:239]
	s_add_u32 s42, s41, 0x1c000
	buffer_load_dwordx4 v[36:39], v1, s[4:7], s42 offen sc0 nt
	v_mfma_f32_16x16x32_bf16 v[240:243], v[80:83], v[116:119], v[240:243]
	s_add_u32 s26, s26, 0x8000
	s_cmp_eq_u32 s26, s32
	s_cselect_b32 s26, s27, s26
	v_mfma_f32_16x16x32_bf16 v[244:247], v[84:87], v[116:119], v[244:247]
	s_barrier
	s_sub_u32 s38, s38, 1
	s_cmp_lg_u32 s38, 0
	s_cbranch_scc1 .Lg_loop0
	v_add_u32_e32 v6, s33, v5
	ds_read_b128 v[72:75], v6 offset:0
	ds_read_b128 v[76:79], v6 offset:2048
	ds_read_b128 v[80:83], v6 offset:4096
	ds_read_b128 v[84:87], v6 offset:6144
	ds_read_b128 v[88:91], v4 offset:0
	ds_read_b128 v[92:95], v4 offset:2048
	ds_read_b128 v[96:99], v4 offset:4096
	ds_read_b128 v[100:103], v4 offset:6144
	ds_read_b128 v[104:107], v4 offset:8192
	ds_read_b128 v[108:111], v4 offset:10240
	ds_read_b128 v[112:115], v4 offset:12288
	ds_read_b128 v[116:119], v4 offset:14336
	s_waitcnt vmcnt(22)
	v_cvt_pk_bf16_f32 v40, v40, v41
	v_cvt_pk_bf16_f32 v41, v42, v43
	v_cvt_pk_bf16_f32 v44, v44, v45
	v_cvt_pk_bf16_f32 v45, v46, v47
	ds_write2st64_b64 v3, v[40:41], v[44:45] offset0:64 offset1:72
	s_waitcnt vmcnt(20)
	v_cvt_pk_bf16_f32 v48, v48, v49
	v_cvt_pk_bf16_f32 v49, v50, v51
	v_cvt_pk_bf16_f32 v52, v52, v53
	v_cvt_pk_bf16_f32 v53, v54, v55
	ds_write2st64_b64 v3, v[48:49], v[52:53] offset0:80 offset1:88
	s_waitcnt vmcnt(16)
	v_cvt_pk_bf16_f32 v56, v56, v57
	v_cvt_pk_bf16_f32 v57, v58, v59
	v_cvt_pk_bf16_f32 v60, v60, v61
	v_cvt_pk_bf16_f32 v61, v62, v63
	ds_write2st64_b64 v3, v[56:57], v[60:61] offset0:96 offset1:104
	s_waitcnt vmcnt(12)
	v_cvt_pk_bf16_f32 v64, v64, v65
	v_cvt_pk_bf16_f32 v65, v66, v67
	v_cvt_pk_bf16_f32 v68, v68, v69
	v_cvt_pk_bf16_f32 v69, v70, v71
	ds_write2st64_b64 v3, v[64:65], v[68:69] offset0:112 offset1:120
	s_waitcnt lgkmcnt(0)
	global_load_dwordx4 v[40:43], v249, s[34:35] offset:0
	global_load_dwordx4 v[44:47], v249, s[34:35] offset:64
	global_load_dwordx4 v[48:51], v249, s[34:35] offset:128
	global_load_dwordx4 v[52:55], v249, s[34:35] offset:192
	s_barrier
	s_mov_b32 m0, s26
	s_min_u32 s40, s25, 31
	s_bitcmp1_b32 s40, 4
	s_cselect_b32 s41, s23, s22
	s_lshl_b32 s42, s40, 23
	s_and_b32 s42, s42, 0x7000000
	s_or_b32 s41, s41, s42
	s_lshl_b32 s42, s40, 8
	s_and_b32 s42, s42, 0x100
	s_or_b32 s41, s41, s42
	s_sub_u32 s43, s25, 1
	s_min_u32 s43, s43, 31
	s_and_b32 s43, s43, 15
	s_lshl_b32 s43, s43, 15
	s_add_u32 s44, s43, s24
	buffer_load_dwordx4 v2, s[12:15], s44 offen sc1 lds
	buffer_load_dwordx4 v2, s[12:15], s44 offen offset:1024 sc1 lds
	buffer_load_dwordx4 v2, s[12:15], s44 offen offset:2048 sc1 lds
	buffer_load_dwordx4 v2, s[12:15], s44 offen offset:3072 sc1 lds
	s_waitcnt vmcnt(4)
	s_mov_b32 s45, s36
	buffer_store_dwordx4 v[120:123], v248, s[28:31], s45 offen
	buffer_store_dwordx4 v[124:127], v248, s[28:31], s45 offen offset:64
	v_mfma_f32_16x16x32_bf16 v[120:123], v[72:75], v[88:91], v[40:43]
	buffer_store_dwordx4 v[128:131], v248, s[28:31], s45 offen offset:128
	v_mfma_f32_16x16x32_bf16 v[124:127], v[76:79], v[88:91], v[44:47]
	buffer_store_dwordx4 v[132:135], v248, s[28:31], s45 offen offset:192
	v_mfma_f32_16x16x32_bf16 v[128:131], v[80:83], v[88:91], v[48:51]
	s_add_u32 s45, s36, 0x2000
	buffer_store_dwordx4 v[136:139], v248, s[28:31], s45 offen
	v_mfma_f32_16x16x32_bf16 v[132:135], v[84:87], v[88:91], v[52:55]
	buffer_store_dwordx4 v[140:143], v248, s[28:31], s45 offen offset:64
	v_mfma_f32_16x16x32_bf16 v[136:139], v[72:75], v[92:95], v[40:43]
	buffer_store_dwordx4 v[144:147], v248, s[28:31], s45 offen offset:128
	v_mfma_f32_16x16x32_bf16 v[140:143], v[76:79], v[92:95], v[44:47]
	buffer_store_dwordx4 v[148:151], v248, s[28:31], s45 offen offset:192
	v_mfma_f32_16x16x32_bf16 v[144:147], v[80:83], v[92:95], v[48:51]
	s_add_u32 s45, s36, 0x4000
	buffer_store_dwordx4 v[152:155], v248, s[28:31], s45 offen
	v_mfma_f32_16x16x32_bf16 v[148:151], v[84:87], v[92:95], v[52:55]
	buffer_store_dwordx4 v[156:159], v248, s[28:31], s45 offen offset:64
	v_mfma_f32_16x16x32_bf16 v[152:155], v[72:75], v[96:99], v[40:43]
	buffer_store_dwordx4 v[160:163], v248, s[28:31], s45 offen offset:128
	v_mfma_f32_16x16x32_bf16 v[156:159], v[76:79], v[96:99], v[44:47]
	buffer_store_dwordx4 v[164:167], v248, s[28:31], s45 offen offset:192
	v_mfma_f32_16x16x32_bf16 v[160:163], v[80:83], v[96:99], v[48:51]
	s_add_u32 s45, s36, 0x6000
	buffer_store_dwordx4 v[168:171], v248, s[28:31], s45 offen
	v_mfma_f32_16x16x32_bf16 v[164:167], v[84:87], v[96:99], v[52:55]
	buffer_store_dwordx4 v[172:175], v248, s[28:31], s45 offen offset:64
	v_mfma_f32_16x16x32_bf16 v[168:171], v[72:75], v[100:103], v[40:43]
	buffer_store_dwordx4 v[176:179], v248, s[28:31], s45 offen offset:128
	v_mfma_f32_16x16x32_bf16 v[172:175], v[76:79], v[100:103], v[44:47]
	buffer_store_dwordx4 v[180:183], v248, s[28:31], s45 offen offset:192
	v_mfma_f32_16x16x32_bf16 v[176:179], v[80:83], v[100:103], v[48:51]
	s_add_u32 s45, s36, 0x8000
	buffer_store_dwordx4 v[184:187], v248, s[28:31], s45 offen
	v_mfma_f32_16x16x32_bf16 v[180:183], v[84:87], v[100:103], v[52:55]
	buffer_store_dwordx4 v[188:191], v248, s[28:31], s45 offen offset:64
	v_mfma_f32_16x16x32_bf16 v[184:187], v[72:75], v[104:107], v[40:43]
	buffer_store_dwordx4 v[192:195], v248, s[28:31], s45 offen offset:128
	v_mfma_f32_16x16x32_bf16 v[188:191], v[76:79], v[104:107], v[44:47]
	buffer_store_dwordx4 v[196:199], v248, s[28:31], s45 offen offset:192
	v_mfma_f32_16x16x32_bf16 v[192:195], v[80:83], v[104:107], v[48:51]
	s_add_u32 s45, s36, 0xa000
	buffer_store_dwordx4 v[200:203], v248, s[28:31], s45 offen
	v_mfma_f32_16x16x32_bf16 v[196:199], v[84:87], v[104:107], v[52:55]
	buffer_store_dwordx4 v[204:207], v248, s[28:31], s45 offen offset:64
	v_mfma_f32_16x16x32_bf16 v[200:203], v[72:75], v[108:111], v[40:43]
	buffer_store_dwordx4 v[208:211], v248, s[28:31], s45 offen offset:128
	v_mfma_f32_16x16x32_bf16 v[204:207], v[76:79], v[108:111], v[44:47]
	buffer_store_dwordx4 v[212:215], v248, s[28:31], s45 offen offset:192
	v_mfma_f32_16x16x32_bf16 v[208:211], v[80:83], v[108:111], v[48:51]
	s_add_u32 s45, s36, 0xc000
	buffer_store_dwordx4 v[216:219], v248, s[28:31], s45 offen
	v_mfma_f32_16x16x32_bf16 v[212:215], v[84:87], v[108:111], v[52:55]
	buffer_store_dwordx4 v[220:223], v248, s[28:31], s45 offen offset:64
	v_mfma_f32_16x16x32_bf16 v[216:219], v[72:75], v[112:115], v[40:43]
	buffer_store_dwordx4 v[224:227], v248, s[28:31], s45 offen offset:128
	v_mfma_f32_16x16x32_bf16 v[220:223], v[76:79], v[112:115], v[44:47]
	buffer_store_dwordx4 v[228:231], v248, s[28:31], s45 offen offset:192
	v_mfma_f32_16x16x32_bf16 v[224:227], v[80:83], v[112:115], v[48:51]
	s_add_u32 s45, s36, 0xe000
	buffer_store_dwordx4 v[232:235], v248, s[28:31], s45 offen
	v_mfma_f32_16x16x32_bf16 v[228:231], v[84:87], v[112:115], v[52:55]
	buffer_store_dwordx4 v[236:239], v248, s[28:31], s45 offen offset:64
	v_mfma_f32_16x16x32_bf16 v[232:235], v[72:75], v[116:119], v[40:43]
	buffer_store_dwordx4 v[240:243], v248, s[28:31], s45 offen offset:128
	v_mfma_f32_16x16x32_bf16 v[236:239], v[76:79], v[116:119], v[44:47]
	buffer_store_dwordx4 v[244:247], v248, s[28:31], s45 offen offset:192
	v_mfma_f32_16x16x32_bf16 v[240:243], v[80:83], v[116:119], v[48:51]
	v_mfma_f32_16x16x32_bf16 v[244:247], v[84:87], v[116:119], v[52:55]
	s_barrier
	ds_read_b128 v[72:75], v6 offset:1024
	ds_read_b128 v[76:79], v6 offset:3072
	ds_read_b128 v[80:83], v6 offset:5120
	ds_read_b128 v[84:87], v6 offset:7168
	ds_read_b128 v[88:91], v4 offset:1024
	ds_read_b128 v[92:95], v4 offset:3072
	ds_read_b128 v[96:99], v4 offset:5120
	ds_read_b128 v[100:103], v4 offset:7168
	ds_read_b128 v[104:107], v4 offset:9216
	ds_read_b128 v[108:111], v4 offset:11264
	ds_read_b128 v[112:115], v4 offset:13312
	ds_read_b128 v[116:119], v4 offset:15360
	s_waitcnt vmcnt(41)
	s_waitcnt lgkmcnt(0)
	s_barrier
	v_mfma_f32_16x16x32_bf16 v[120:123], v[72:75], v[88:91], v[120:123]
	s_add_u32 s33, s33, 0x8000
	s_cmp_eq_u32 s33, 0x18000
	s_cselect_b32 s33, 0, s33
	s_add_u32 s25, s25, 1
	v_mfma_f32_16x16x32_bf16 v[124:127], v[76:79], v[88:91], v[124:127]
	v_mfma_f32_16x16x32_bf16 v[128:131], v[80:83], v[88:91], v[128:131]
	buffer_load_dwordx4 v[40:43], v1, s[4:7], s41 offen sc0 nt
	v_mfma_f32_16x16x32_bf16 v[132:135], v[84:87], v[88:91], v[132:135]
	v_mfma_f32_16x16x32_bf16 v[136:139], v[72:75], v[92:95], v[136:139]
	v_mfma_f32_16x16x32_bf16 v[140:143], v[76:79], v[92:95], v[140:143]
	v_mfma_f32_16x16x32_bf16 v[144:147], v[80:83], v[92:95], v[144:147]
	s_add_u32 s42, s41, 0x4000
	buffer_load_dwordx4 v[44:47], v1, s[4:7], s42 offen sc0 nt
	v_mfma_f32_16x16x32_bf16 v[148:151], v[84:87], v[92:95], v[148:151]
	v_mfma_f32_16x16x32_bf16 v[152:155], v[72:75], v[96:99], v[152:155]
	v_mfma_f32_16x16x32_bf16 v[156:159], v[76:79], v[96:99], v[156:159]
	v_mfma_f32_16x16x32_bf16 v[160:163], v[80:83], v[96:99], v[160:163]
	s_add_u32 s42, s41, 0x8000
	buffer_load_dwordx4 v[48:51], v1, s[4:7], s42 offen sc0 nt
	v_mfma_f32_16x16x32_bf16 v[164:167], v[84:87], v[96:99], v[164:167]
	v_mfma_f32_16x16x32_bf16 v[168:171], v[72:75], v[100:103], v[168:171]
	v_mfma_f32_16x16x32_bf16 v[172:175], v[76:79], v[100:103], v[172:175]
	v_mfma_f32_16x16x32_bf16 v[176:179], v[80:83], v[100:103], v[176:179]
	s_add_u32 s42, s41, 0xc000
	buffer_load_dwordx4 v[52:55], v1, s[4:7], s42 offen sc0 nt
	v_mfma_f32_16x16x32_bf16 v[180:183], v[84:87], v[100:103], v[180:183]
	v_mfma_f32_16x16x32_bf16 v[184:187], v[72:75], v[104:107], v[184:187]
	v_mfma_f32_16x16x32_bf16 v[188:191], v[76:79], v[104:107], v[188:191]
	v_mfma_f32_16x16x32_bf16 v[192:195], v[80:83], v[104:107], v[192:195]
	s_add_u32 s42, s41, 0x10000
	buffer_load_dwordx4 v[56:59], v1, s[4:7], s42 offen sc0 nt
	v_mfma_f32_16x16x32_bf16 v[196:199], v[84:87], v[104:107], v[196:199]
	v_mfma_f32_16x16x32_bf16 v[200:203], v[72:75], v[108:111], v[200:203]
	v_mfma_f32_16x16x32_bf16 v[204:207], v[76:79], v[108:111], v[204:207]
	v_mfma_f32_16x16x32_bf16 v[208:211], v[80:83], v[108:111], v[208:211]
	s_add_u32 s42, s41, 0x14000
	buffer_load_dwordx4 v[60:63], v1, s[4:7], s42 offen sc0 nt
	v_mfma_f32_16x16x32_bf16 v[212:215], v[84:87], v[108:111], v[212:215]
	v_mfma_f32_16x16x32_bf16 v[216:219], v[72:75], v[112:115], v[216:219]
	v_mfma_f32_16x16x32_bf16 v[220:223], v[76:79], v[112:115], v[220:223]
	v_mfma_f32_16x16x32_bf16 v[224:227], v[80:83], v[112:115], v[224:227]
	s_add_u32 s42, s41, 0x18000
	buffer_load_dwordx4 v[64:67], v1, s[4:7], s42 offen sc0 nt
	v_mfma_f32_16x16x32_bf16 v[228:231], v[84:87], v[112:115], v[228:231]
	v_mfma_f32_16x16x32_bf16 v[232:235], v[72:75], v[116:119], v[232:235]
	v_mfma_f32_16x16x32_bf16 v[236:239], v[76:79], v[116:119], v[236:239]
	v_mfma_f32_16x16x32_bf16 v[240:243], v[80:83], v[116:119], v[240:243]
	s_add_u32 s42, s41, 0x1c000
	buffer_load_dwordx4 v[68:71], v1, s[4:7], s42 offen sc0 nt
	s_add_u32 s26, s26, 0x8000
	s_cmp_eq_u32 s26, s32
	s_cselect_b32 s26, s27, s26
	v_mfma_f32_16x16x32_bf16 v[244:247], v[84:87], v[116:119], v[244:247]
	s_barrier
	v_add_u32_e32 v6, s33, v5
	ds_read_b128 v[72:75], v6 offset:0
	ds_read_b128 v[76:79], v6 offset:2048
	ds_read_b128 v[80:83], v6 offset:4096
	ds_read_b128 v[84:87], v6 offset:6144
	ds_read_b128 v[88:91], v4 offset:32768
	ds_read_b128 v[92:95], v4 offset:34816
	ds_read_b128 v[96:99], v4 offset:36864
	ds_read_b128 v[100:103], v4 offset:38912
	ds_read_b128 v[104:107], v4 offset:40960
	ds_read_b128 v[108:111], v4 offset:43008
	ds_read_b128 v[112:115], v4 offset:45056
	ds_read_b128 v[116:119], v4 offset:47104
	s_waitcnt vmcnt(58)
	v_cvt_pk_bf16_f32 v8, v8, v9
	v_cvt_pk_bf16_f32 v9, v10, v11
	v_cvt_pk_bf16_f32 v12, v12, v13
	v_cvt_pk_bf16_f32 v13, v14, v15
	ds_write2st64_b64 v3, v[8:9], v[12:13] offset0:0 offset1:8
	s_waitcnt vmcnt(56)
	v_cvt_pk_bf16_f32 v16, v16, v17
	v_cvt_pk_bf16_f32 v17, v18, v19
	v_cvt_pk_bf16_f32 v20, v20, v21
	v_cvt_pk_bf16_f32 v21, v22, v23
	ds_write2st64_b64 v3, v[16:17], v[20:21] offset0:16 offset1:24
	s_waitcnt vmcnt(52)
	v_cvt_pk_bf16_f32 v24, v24, v25
	v_cvt_pk_bf16_f32 v25, v26, v27
	v_cvt_pk_bf16_f32 v28, v28, v29
	v_cvt_pk_bf16_f32 v29, v30, v31
	ds_write2st64_b64 v3, v[24:25], v[28:29] offset0:32 offset1:40
	s_waitcnt vmcnt(48)
	v_cvt_pk_bf16_f32 v32, v32, v33
	v_cvt_pk_bf16_f32 v33, v34, v35
	v_cvt_pk_bf16_f32 v36, v36, v37
	v_cvt_pk_bf16_f32 v37, v38, v39
	ds_write2st64_b64 v3, v[32:33], v[36:37] offset0:48 offset1:56
	s_waitcnt lgkmcnt(0)
	s_barrier
	v_mfma_f32_16x16x32_bf16 v[120:123], v[72:75], v[88:91], v[120:123]
	s_min_u32 s40, s25, 31
	s_bitcmp1_b32 s40, 4
	s_cselect_b32 s41, s23, s22
	s_lshl_b32 s42, s40, 23
	s_and_b32 s42, s42, 0x7000000
	s_or_b32 s41, s41, s42
	s_lshl_b32 s42, s40, 8
	s_and_b32 s42, s42, 0x100
	s_or_b32 s41, s41, s42
	s_sub_u32 s43, s25, 1
	s_min_u32 s43, s43, 31
	s_and_b32 s43, s43, 15
	s_lshl_b32 s43, s43, 15
	s_add_u32 s44, s43, s24
	v_mfma_f32_16x16x32_bf16 v[124:127], v[76:79], v[88:91], v[124:127]
	v_mfma_f32_16x16x32_bf16 v[128:131], v[80:83], v[88:91], v[128:131]
	v_mfma_f32_16x16x32_bf16 v[132:135], v[84:87], v[88:91], v[132:135]
	buffer_load_dwordx4 v[8:11], v1, s[4:7], s41 offen sc0 nt
	v_mfma_f32_16x16x32_bf16 v[136:139], v[72:75], v[92:95], v[136:139]
	v_mfma_f32_16x16x32_bf16 v[140:143], v[76:79], v[92:95], v[140:143]
	v_mfma_f32_16x16x32_bf16 v[144:147], v[80:83], v[92:95], v[144:147]
	v_mfma_f32_16x16x32_bf16 v[148:151], v[84:87], v[92:95], v[148:151]
	v_mfma_f32_16x16x32_bf16 v[152:155], v[72:75], v[96:99], v[152:155]
	v_mfma_f32_16x16x32_bf16 v[156:159], v[76:79], v[96:99], v[156:159]
	v_mfma_f32_16x16x32_bf16 v[160:163], v[80:83], v[96:99], v[160:163]
	v_mfma_f32_16x16x32_bf16 v[164:167], v[84:87], v[96:99], v[164:167]
	s_add_u32 s42, s41, 0x4000
	buffer_load_dwordx4 v[12:15], v1, s[4:7], s42 offen sc0 nt
	v_mfma_f32_16x16x32_bf16 v[168:171], v[72:75], v[100:103], v[168:171]
	v_mfma_f32_16x16x32_bf16 v[172:175], v[76:79], v[100:103], v[172:175]
	v_mfma_f32_16x16x32_bf16 v[176:179], v[80:83], v[100:103], v[176:179]
	v_mfma_f32_16x16x32_bf16 v[180:183], v[84:87], v[100:103], v[180:183]
	v_mfma_f32_16x16x32_bf16 v[184:187], v[72:75], v[104:107], v[184:187]
	v_mfma_f32_16x16x32_bf16 v[188:191], v[76:79], v[104:107], v[188:191]
	v_mfma_f32_16x16x32_bf16 v[192:195], v[80:83], v[104:107], v[192:195]
	v_mfma_f32_16x16x32_bf16 v[196:199], v[84:87], v[104:107], v[196:199]
	s_add_u32 s42, s41, 0x8000
	buffer_load_dwordx4 v[16:19], v1, s[4:7], s42 offen sc0 nt
	v_mfma_f32_16x16x32_bf16 v[200:203], v[72:75], v[108:111], v[200:203]
	v_mfma_f32_16x16x32_bf16 v[204:207], v[76:79], v[108:111], v[204:207]
	v_mfma_f32_16x16x32_bf16 v[208:211], v[80:83], v[108:111], v[208:211]
	v_mfma_f32_16x16x32_bf16 v[212:215], v[84:87], v[108:111], v[212:215]
	v_mfma_f32_16x16x32_bf16 v[216:219], v[72:75], v[112:115], v[216:219]
	v_mfma_f32_16x16x32_bf16 v[220:223], v[76:79], v[112:115], v[220:223]
	v_mfma_f32_16x16x32_bf16 v[224:227], v[80:83], v[112:115], v[224:227]
	v_mfma_f32_16x16x32_bf16 v[228:231], v[84:87], v[112:115], v[228:231]
	s_add_u32 s42, s41, 0xc000
	buffer_load_dwordx4 v[20:23], v1, s[4:7], s42 offen sc0 nt
	v_mfma_f32_16x16x32_bf16 v[232:235], v[72:75], v[116:119], v[232:235]
	v_mfma_f32_16x16x32_bf16 v[236:239], v[76:79], v[116:119], v[236:239]
	v_mfma_f32_16x16x32_bf16 v[240:243], v[80:83], v[116:119], v[240:243]
	v_mfma_f32_16x16x32_bf16 v[244:247], v[84:87], v[116:119], v[244:247]
	s_barrier
	ds_read_b128 v[72:75], v6 offset:1024
	ds_read_b128 v[76:79], v6 offset:3072
	ds_read_b128 v[80:83], v6 offset:5120
	ds_read_b128 v[84:87], v6 offset:7168
	ds_read_b128 v[88:91], v4 offset:33792
	ds_read_b128 v[92:95], v4 offset:35840
	ds_read_b128 v[96:99], v4 offset:37888
	ds_read_b128 v[100:103], v4 offset:39936
	ds_read_b128 v[104:107], v4 offset:41984
	ds_read_b128 v[108:111], v4 offset:44032
	ds_read_b128 v[112:115], v4 offset:46080
	ds_read_b128 v[116:119], v4 offset:48128
	s_waitcnt vmcnt(44)
	s_waitcnt lgkmcnt(0)
	s_barrier
	v_mfma_f32_16x16x32_bf16 v[120:123], v[72:75], v[88:91], v[120:123]
	s_add_u32 s33, s33, 0x8000
	s_cmp_eq_u32 s33, 0x18000
	s_cselect_b32 s33, 0, s33
	s_add_u32 s25, s25, 1
	s_mov_b32 m0, s26
	v_mfma_f32_16x16x32_bf16 v[124:127], v[76:79], v[88:91], v[124:127]
	buffer_load_dwordx4 v2, s[12:15], s44 offen sc1 lds
	v_mfma_f32_16x16x32_bf16 v[128:131], v[80:83], v[88:91], v[128:131]
	v_mfma_f32_16x16x32_bf16 v[132:135], v[84:87], v[88:91], v[132:135]
	v_mfma_f32_16x16x32_bf16 v[136:139], v[72:75], v[92:95], v[136:139]
	v_mfma_f32_16x16x32_bf16 v[140:143], v[76:79], v[92:95], v[140:143]
	s_add_u32 s42, s41, 0x10000
	buffer_load_dwordx4 v[24:27], v1, s[4:7], s42 offen sc0 nt
	v_mfma_f32_16x16x32_bf16 v[144:147], v[80:83], v[92:95], v[144:147]
	v_mfma_f32_16x16x32_bf16 v[148:151], v[84:87], v[92:95], v[148:151]
	v_mfma_f32_16x16x32_bf16 v[152:155], v[72:75], v[96:99], v[152:155]
	v_mfma_f32_16x16x32_bf16 v[156:159], v[76:79], v[96:99], v[156:159]
	buffer_load_dwordx4 v2, s[12:15], s44 offen offset:1024 sc1 lds
	v_mfma_f32_16x16x32_bf16 v[160:163], v[80:83], v[96:99], v[160:163]
	v_mfma_f32_16x16x32_bf16 v[164:167], v[84:87], v[96:99], v[164:167]
	v_mfma_f32_16x16x32_bf16 v[168:171], v[72:75], v[100:103], v[168:171]
	v_mfma_f32_16x16x32_bf16 v[172:175], v[76:79], v[100:103], v[172:175]
	s_add_u32 s42, s41, 0x14000
	buffer_load_dwordx4 v[28:31], v1, s[4:7], s42 offen sc0 nt
	v_mfma_f32_16x16x32_bf16 v[176:179], v[80:83], v[100:103], v[176:179]
	v_mfma_f32_16x16x32_bf16 v[180:183], v[84:87], v[100:103], v[180:183]
	v_mfma_f32_16x16x32_bf16 v[184:187], v[72:75], v[104:107], v[184:187]
	v_mfma_f32_16x16x32_bf16 v[188:191], v[76:79], v[104:107], v[188:191]
	buffer_load_dwordx4 v2, s[12:15], s44 offen offset:2048 sc1 lds
	v_mfma_f32_16x16x32_bf16 v[192:195], v[80:83], v[104:107], v[192:195]
	v_mfma_f32_16x16x32_bf16 v[196:199], v[84:87], v[104:107], v[196:199]
	v_mfma_f32_16x16x32_bf16 v[200:203], v[72:75], v[108:111], v[200:203]
	v_mfma_f32_16x16x32_bf16 v[204:207], v[76:79], v[108:111], v[204:207]
	s_add_u32 s42, s41, 0x18000
	buffer_load_dwordx4 v[32:35], v1, s[4:7], s42 offen sc0 nt
	v_mfma_f32_16x16x32_bf16 v[208:211], v[80:83], v[108:111], v[208:211]
	v_mfma_f32_16x16x32_bf16 v[212:215], v[84:87], v[108:111], v[212:215]
	v_mfma_f32_16x16x32_bf16 v[216:219], v[72:75], v[112:115], v[216:219]
	v_mfma_f32_16x16x32_bf16 v[220:223], v[76:79], v[112:115], v[220:223]
	buffer_load_dwordx4 v2, s[12:15], s44 offen offset:3072 sc1 lds
	v_mfma_f32_16x16x32_bf16 v[224:227], v[80:83], v[112:115], v[224:227]
	v_mfma_f32_16x16x32_bf16 v[228:231], v[84:87], v[112:115], v[228:231]
	v_mfma_f32_16x16x32_bf16 v[232:235], v[72:75], v[116:119], v[232:235]
	v_mfma_f32_16x16x32_bf16 v[236:239], v[76:79], v[116:119], v[236:239]
	s_add_u32 s42, s41, 0x1c000
	buffer_load_dwordx4 v[36:39], v1, s[4:7], s42 offen sc0 nt
	v_mfma_f32_16x16x32_bf16 v[240:243], v[80:83], v[116:119], v[240:243]
	s_add_u32 s26, s26, 0x8000
	s_cmp_eq_u32 s26, s32
	s_cselect_b32 s26, s27, s26
	v_mfma_f32_16x16x32_bf16 v[244:247], v[84:87], v[116:119], v[244:247]
	s_barrier
	v_add_u32_e32 v6, s33, v5
	ds_read_b128 v[72:75], v6 offset:0
	ds_read_b128 v[76:79], v6 offset:2048
	ds_read_b128 v[80:83], v6 offset:4096
	ds_read_b128 v[84:87], v6 offset:6144
	ds_read_b128 v[88:91], v4 offset:0
	ds_read_b128 v[92:95], v4 offset:2048
	ds_read_b128 v[96:99], v4 offset:4096
	ds_read_b128 v[100:103], v4 offset:6144
	ds_read_b128 v[104:107], v4 offset:8192
	ds_read_b128 v[108:111], v4 offset:10240
	ds_read_b128 v[112:115], v4 offset:12288
	ds_read_b128 v[116:119], v4 offset:14336
	s_waitcnt vmcnt(18)
	v_cvt_pk_bf16_f32 v40, v40, v41
	v_cvt_pk_bf16_f32 v41, v42, v43
	v_cvt_pk_bf16_f32 v44, v44, v45
	v_cvt_pk_bf16_f32 v45, v46, v47
	ds_write2st64_b64 v3, v[40:41], v[44:45] offset0:64 offset1:72
	s_waitcnt vmcnt(16)
	v_cvt_pk_bf16_f32 v48, v48, v49
	v_cvt_pk_bf16_f32 v49, v50, v51
	v_cvt_pk_bf16_f32 v52, v52, v53
	v_cvt_pk_bf16_f32 v53, v54, v55
	ds_write2st64_b64 v3, v[48:49], v[52:53] offset0:80 offset1:88
	s_waitcnt vmcnt(14)
	v_cvt_pk_bf16_f32 v56, v56, v57
	v_cvt_pk_bf16_f32 v57, v58, v59
	v_cvt_pk_bf16_f32 v60, v60, v61
	v_cvt_pk_bf16_f32 v61, v62, v63
	ds_write2st64_b64 v3, v[56:57], v[60:61] offset0:96 offset1:104
	s_waitcnt vmcnt(12)
	v_cvt_pk_bf16_f32 v64, v64, v65
	v_cvt_pk_bf16_f32 v65, v66, v67
	v_cvt_pk_bf16_f32 v68, v68, v69
	v_cvt_pk_bf16_f32 v69, v70, v71
	ds_write2st64_b64 v3, v[64:65], v[68:69] offset0:112 offset1:120
	s_waitcnt lgkmcnt(0)
	s_barrier
	v_mfma_f32_16x16x32_bf16 v[120:123], v[72:75], v[88:91], v[120:123]
	s_min_u32 s40, s25, 31
	s_bitcmp1_b32 s40, 4
	s_cselect_b32 s41, s23, s22
	s_lshl_b32 s42, s40, 23
	s_and_b32 s42, s42, 0x7000000
	s_or_b32 s41, s41, s42
	s_lshl_b32 s42, s40, 8
	s_and_b32 s42, s42, 0x100
	s_or_b32 s41, s41, s42
	s_sub_u32 s43, s25, 1
	s_min_u32 s43, s43, 31
	s_and_b32 s43, s43, 15
	s_lshl_b32 s43, s43, 15
	s_add_u32 s44, s43, s24
	v_mfma_f32_16x16x32_bf16 v[124:127], v[76:79], v[88:91], v[124:127]
	v_mfma_f32_16x16x32_bf16 v[128:131], v[80:83], v[88:91], v[128:131]
	v_mfma_f32_16x16x32_bf16 v[132:135], v[84:87], v[88:91], v[132:135]
	buffer_load_dwordx4 v[40:43], v1, s[4:7], s41 offen sc0 nt
	v_mfma_f32_16x16x32_bf16 v[136:139], v[72:75], v[92:95], v[136:139]
	v_mfma_f32_16x16x32_bf16 v[140:143], v[76:79], v[92:95], v[140:143]
	v_mfma_f32_16x16x32_bf16 v[144:147], v[80:83], v[92:95], v[144:147]
	v_mfma_f32_16x16x32_bf16 v[148:151], v[84:87], v[92:95], v[148:151]
	v_mfma_f32_16x16x32_bf16 v[152:155], v[72:75], v[96:99], v[152:155]
	v_mfma_f32_16x16x32_bf16 v[156:159], v[76:79], v[96:99], v[156:159]
	v_mfma_f32_16x16x32_bf16 v[160:163], v[80:83], v[96:99], v[160:163]
	v_mfma_f32_16x16x32_bf16 v[164:167], v[84:87], v[96:99], v[164:167]
	s_add_u32 s42, s41, 0x4000
	buffer_load_dwordx4 v[44:47], v1, s[4:7], s42 offen sc0 nt
	v_mfma_f32_16x16x32_bf16 v[168:171], v[72:75], v[100:103], v[168:171]
	v_mfma_f32_16x16x32_bf16 v[172:175], v[76:79], v[100:103], v[172:175]
	v_mfma_f32_16x16x32_bf16 v[176:179], v[80:83], v[100:103], v[176:179]
	v_mfma_f32_16x16x32_bf16 v[180:183], v[84:87], v[100:103], v[180:183]
	v_mfma_f32_16x16x32_bf16 v[184:187], v[72:75], v[104:107], v[184:187]
	v_mfma_f32_16x16x32_bf16 v[188:191], v[76:79], v[104:107], v[188:191]
	v_mfma_f32_16x16x32_bf16 v[192:195], v[80:83], v[104:107], v[192:195]
	v_mfma_f32_16x16x32_bf16 v[196:199], v[84:87], v[104:107], v[196:199]
	s_add_u32 s42, s41, 0x8000
	buffer_load_dwordx4 v[48:51], v1, s[4:7], s42 offen sc0 nt
	v_mfma_f32_16x16x32_bf16 v[200:203], v[72:75], v[108:111], v[200:203]
	v_mfma_f32_16x16x32_bf16 v[204:207], v[76:79], v[108:111], v[204:207]
	v_mfma_f32_16x16x32_bf16 v[208:211], v[80:83], v[108:111], v[208:211]
	v_mfma_f32_16x16x32_bf16 v[212:215], v[84:87], v[108:111], v[212:215]
	v_mfma_f32_16x16x32_bf16 v[216:219], v[72:75], v[112:115], v[216:219]
	v_mfma_f32_16x16x32_bf16 v[220:223], v[76:79], v[112:115], v[220:223]
	v_mfma_f32_16x16x32_bf16 v[224:227], v[80:83], v[112:115], v[224:227]
	v_mfma_f32_16x16x32_bf16 v[228:231], v[84:87], v[112:115], v[228:231]
	s_add_u32 s42, s41, 0xc000
	buffer_load_dwordx4 v[52:55], v1, s[4:7], s42 offen sc0 nt
	v_mfma_f32_16x16x32_bf16 v[232:235], v[72:75], v[116:119], v[232:235]
	v_mfma_f32_16x16x32_bf16 v[236:239], v[76:79], v[116:119], v[236:239]
	v_mfma_f32_16x16x32_bf16 v[240:243], v[80:83], v[116:119], v[240:243]
	v_mfma_f32_16x16x32_bf16 v[244:247], v[84:87], v[116:119], v[244:247]
	s_barrier
	ds_read_b128 v[72:75], v6 offset:1024
	ds_read_b128 v[76:79], v6 offset:3072
	ds_read_b128 v[80:83], v6 offset:5120
	ds_read_b128 v[84:87], v6 offset:7168
	ds_read_b128 v[88:91], v4 offset:1024
	ds_read_b128 v[92:95], v4 offset:3072
	ds_read_b128 v[96:99], v4 offset:5120
	ds_read_b128 v[100:103], v4 offset:7168
	ds_read_b128 v[104:107], v4 offset:9216
	ds_read_b128 v[108:111], v4 offset:11264
	ds_read_b128 v[112:115], v4 offset:13312
	ds_read_b128 v[116:119], v4 offset:15360
	s_waitcnt vmcnt(5)
	s_waitcnt lgkmcnt(0)
	s_barrier
	v_mfma_f32_16x16x32_bf16 v[120:123], v[72:75], v[88:91], v[120:123]
	s_add_u32 s33, s33, 0x8000
	s_cmp_eq_u32 s33, 0x18000
	s_cselect_b32 s33, 0, s33
	s_add_u32 s25, s25, 1
	s_mov_b32 m0, s26
	v_mfma_f32_16x16x32_bf16 v[124:127], v[76:79], v[88:91], v[124:127]
	buffer_load_dwordx4 v2, s[12:15], s44 offen sc1 lds
	v_mfma_f32_16x16x32_bf16 v[128:131], v[80:83], v[88:91], v[128:131]
	v_mfma_f32_16x16x32_bf16 v[132:135], v[84:87], v[88:91], v[132:135]
	v_mfma_f32_16x16x32_bf16 v[136:139], v[72:75], v[92:95], v[136:139]
	v_mfma_f32_16x16x32_bf16 v[140:143], v[76:79], v[92:95], v[140:143]
	s_add_u32 s42, s41, 0x10000
	buffer_load_dwordx4 v[56:59], v1, s[4:7], s42 offen sc0 nt
	v_mfma_f32_16x16x32_bf16 v[144:147], v[80:83], v[92:95], v[144:147]
	v_mfma_f32_16x16x32_bf16 v[148:151], v[84:87], v[92:95], v[148:151]
	v_mfma_f32_16x16x32_bf16 v[152:155], v[72:75], v[96:99], v[152:155]
	v_mfma_f32_16x16x32_bf16 v[156:159], v[76:79], v[96:99], v[156:159]
	buffer_load_dwordx4 v2, s[12:15], s44 offen offset:1024 sc1 lds
	v_mfma_f32_16x16x32_bf16 v[160:163], v[80:83], v[96:99], v[160:163]
	v_mfma_f32_16x16x32_bf16 v[164:167], v[84:87], v[96:99], v[164:167]
	v_mfma_f32_16x16x32_bf16 v[168:171], v[72:75], v[100:103], v[168:171]
	v_mfma_f32_16x16x32_bf16 v[172:175], v[76:79], v[100:103], v[172:175]
	s_add_u32 s42, s41, 0x14000
	buffer_load_dwordx4 v[60:63], v1, s[4:7], s42 offen sc0 nt
	v_mfma_f32_16x16x32_bf16 v[176:179], v[80:83], v[100:103], v[176:179]
	v_mfma_f32_16x16x32_bf16 v[180:183], v[84:87], v[100:103], v[180:183]
	v_mfma_f32_16x16x32_bf16 v[184:187], v[72:75], v[104:107], v[184:187]
	v_mfma_f32_16x16x32_bf16 v[188:191], v[76:79], v[104:107], v[188:191]
	buffer_load_dwordx4 v2, s[12:15], s44 offen offset:2048 sc1 lds
	v_mfma_f32_16x16x32_bf16 v[192:195], v[80:83], v[104:107], v[192:195]
	v_mfma_f32_16x16x32_bf16 v[196:199], v[84:87], v[104:107], v[196:199]
	v_mfma_f32_16x16x32_bf16 v[200:203], v[72:75], v[108:111], v[200:203]
	v_mfma_f32_16x16x32_bf16 v[204:207], v[76:79], v[108:111], v[204:207]
	s_add_u32 s42, s41, 0x18000
	buffer_load_dwordx4 v[64:67], v1, s[4:7], s42 offen sc0 nt
	v_mfma_f32_16x16x32_bf16 v[208:211], v[80:83], v[108:111], v[208:211]
	v_mfma_f32_16x16x32_bf16 v[212:215], v[84:87], v[108:111], v[212:215]
	v_mfma_f32_16x16x32_bf16 v[216:219], v[72:75], v[112:115], v[216:219]
	v_mfma_f32_16x16x32_bf16 v[220:223], v[76:79], v[112:115], v[220:223]
	buffer_load_dwordx4 v2, s[12:15], s44 offen offset:3072 sc1 lds
	v_mfma_f32_16x16x32_bf16 v[224:227], v[80:83], v[112:115], v[224:227]
	v_mfma_f32_16x16x32_bf16 v[228:231], v[84:87], v[112:115], v[228:231]
	v_mfma_f32_16x16x32_bf16 v[232:235], v[72:75], v[116:119], v[232:235]
	v_mfma_f32_16x16x32_bf16 v[236:239], v[76:79], v[116:119], v[236:239]
	s_add_u32 s42, s41, 0x1c000
	buffer_load_dwordx4 v[68:71], v1, s[4:7], s42 offen sc0 nt
	v_mfma_f32_16x16x32_bf16 v[240:243], v[80:83], v[116:119], v[240:243]
	s_add_u32 s26, s26, 0x8000
	s_cmp_eq_u32 s26, s32
	s_cselect_b32 s26, s27, s26
	v_mfma_f32_16x16x32_bf16 v[244:247], v[84:87], v[116:119], v[244:247]
	s_barrier
	v_add_u32_e32 v6, s33, v5
	ds_read_b128 v[72:75], v6 offset:0
	ds_read_b128 v[76:79], v6 offset:2048
	ds_read_b128 v[80:83], v6 offset:4096
	ds_read_b128 v[84:87], v6 offset:6144
	ds_read_b128 v[88:91], v4 offset:32768
	ds_read_b128 v[92:95], v4 offset:34816
	ds_read_b128 v[96:99], v4 offset:36864
	ds_read_b128 v[100:103], v4 offset:38912
	ds_read_b128 v[104:107], v4 offset:40960
	ds_read_b128 v[108:111], v4 offset:43008
	ds_read_b128 v[112:115], v4 offset:45056
	ds_read_b128 v[116:119], v4 offset:47104
	s_waitcnt vmcnt(22)
	v_cvt_pk_bf16_f32 v8, v8, v9
	v_cvt_pk_bf16_f32 v9, v10, v11
	v_cvt_pk_bf16_f32 v12, v12, v13
	v_cvt_pk_bf16_f32 v13, v14, v15
	ds_write2st64_b64 v3, v[8:9], v[12:13] offset0:0 offset1:8
	s_waitcnt vmcnt(20)
	v_cvt_pk_bf16_f32 v16, v16, v17
	v_cvt_pk_bf16_f32 v17, v18, v19
	v_cvt_pk_bf16_f32 v20, v20, v21
	v_cvt_pk_bf16_f32 v21, v22, v23
	ds_write2st64_b64 v3, v[16:17], v[20:21] offset0:16 offset1:24
	s_waitcnt vmcnt(16)
	v_cvt_pk_bf16_f32 v24, v24, v25
	v_cvt_pk_bf16_f32 v25, v26, v27
	v_cvt_pk_bf16_f32 v28, v28, v29
	v_cvt_pk_bf16_f32 v29, v30, v31
	ds_write2st64_b64 v3, v[24:25], v[28:29] offset0:32 offset1:40
	s_waitcnt vmcnt(12)
	v_cvt_pk_bf16_f32 v32, v32, v33
	v_cvt_pk_bf16_f32 v33, v34, v35
	v_cvt_pk_bf16_f32 v36, v36, v37
	v_cvt_pk_bf16_f32 v37, v38, v39
	ds_write2st64_b64 v3, v[32:33], v[36:37] offset0:48 offset1:56
	s_waitcnt lgkmcnt(0)
	s_barrier
	v_mfma_f32_16x16x32_bf16 v[120:123], v[72:75], v[88:91], v[120:123]
	s_min_u32 s40, s25, 31
	s_bitcmp1_b32 s40, 4
	s_cselect_b32 s41, s23, s22
	s_lshl_b32 s42, s40, 23
	s_and_b32 s42, s42, 0x7000000
	s_or_b32 s41, s41, s42
	s_lshl_b32 s42, s40, 8
	s_and_b32 s42, s42, 0x100
	s_or_b32 s41, s41, s42
	s_sub_u32 s43, s25, 1
	s_min_u32 s43, s43, 31
	s_and_b32 s43, s43, 15
	s_lshl_b32 s43, s43, 15
	s_add_u32 s44, s43, s24
	v_mfma_f32_16x16x32_bf16 v[124:127], v[76:79], v[88:91], v[124:127]
	v_mfma_f32_16x16x32_bf16 v[128:131], v[80:83], v[88:91], v[128:131]
	v_mfma_f32_16x16x32_bf16 v[132:135], v[84:87], v[88:91], v[132:135]
	buffer_load_dwordx4 v[8:11], v1, s[4:7], s41 offen sc0 nt
	v_mfma_f32_16x16x32_bf16 v[136:139], v[72:75], v[92:95], v[136:139]
	v_mfma_f32_16x16x32_bf16 v[140:143], v[76:79], v[92:95], v[140:143]
	v_mfma_f32_16x16x32_bf16 v[144:147], v[80:83], v[92:95], v[144:147]
	v_mfma_f32_16x16x32_bf16 v[148:151], v[84:87], v[92:95], v[148:151]
	v_mfma_f32_16x16x32_bf16 v[152:155], v[72:75], v[96:99], v[152:155]
	v_mfma_f32_16x16x32_bf16 v[156:159], v[76:79], v[96:99], v[156:159]
	v_mfma_f32_16x16x32_bf16 v[160:163], v[80:83], v[96:99], v[160:163]
	v_mfma_f32_16x16x32_bf16 v[164:167], v[84:87], v[96:99], v[164:167]
	s_add_u32 s42, s41, 0x4000
	buffer_load_dwordx4 v[12:15], v1, s[4:7], s42 offen sc0 nt
	v_mfma_f32_16x16x32_bf16 v[168:171], v[72:75], v[100:103], v[168:171]
	v_mfma_f32_16x16x32_bf16 v[172:175], v[76:79], v[100:103], v[172:175]
	v_mfma_f32_16x16x32_bf16 v[176:179], v[80:83], v[100:103], v[176:179]
	v_mfma_f32_16x16x32_bf16 v[180:183], v[84:87], v[100:103], v[180:183]
	v_mfma_f32_16x16x32_bf16 v[184:187], v[72:75], v[104:107], v[184:187]
	v_mfma_f32_16x16x32_bf16 v[188:191], v[76:79], v[104:107], v[188:191]
	v_mfma_f32_16x16x32_bf16 v[192:195], v[80:83], v[104:107], v[192:195]
	v_mfma_f32_16x16x32_bf16 v[196:199], v[84:87], v[104:107], v[196:199]
	s_add_u32 s42, s41, 0x8000
	buffer_load_dwordx4 v[16:19], v1, s[4:7], s42 offen sc0 nt
	v_mfma_f32_16x16x32_bf16 v[200:203], v[72:75], v[108:111], v[200:203]
	v_mfma_f32_16x16x32_bf16 v[204:207], v[76:79], v[108:111], v[204:207]
	v_mfma_f32_16x16x32_bf16 v[208:211], v[80:83], v[108:111], v[208:211]
	v_mfma_f32_16x16x32_bf16 v[212:215], v[84:87], v[108:111], v[212:215]
	v_mfma_f32_16x16x32_bf16 v[216:219], v[72:75], v[112:115], v[216:219]
	v_mfma_f32_16x16x32_bf16 v[220:223], v[76:79], v[112:115], v[220:223]
	v_mfma_f32_16x16x32_bf16 v[224:227], v[80:83], v[112:115], v[224:227]
	v_mfma_f32_16x16x32_bf16 v[228:231], v[84:87], v[112:115], v[228:231]
	s_add_u32 s42, s41, 0xc000
	buffer_load_dwordx4 v[20:23], v1, s[4:7], s42 offen sc0 nt
	v_mfma_f32_16x16x32_bf16 v[232:235], v[72:75], v[116:119], v[232:235]
	v_mfma_f32_16x16x32_bf16 v[236:239], v[76:79], v[116:119], v[236:239]
	v_mfma_f32_16x16x32_bf16 v[240:243], v[80:83], v[116:119], v[240:243]
	v_mfma_f32_16x16x32_bf16 v[244:247], v[84:87], v[116:119], v[244:247]
	s_barrier
	ds_read_b128 v[72:75], v6 offset:1024
	ds_read_b128 v[76:79], v6 offset:3072
	ds_read_b128 v[80:83], v6 offset:5120
	ds_read_b128 v[84:87], v6 offset:7168
	ds_read_b128 v[88:91], v4 offset:33792
	ds_read_b128 v[92:95], v4 offset:35840
	ds_read_b128 v[96:99], v4 offset:37888
	ds_read_b128 v[100:103], v4 offset:39936
	ds_read_b128 v[104:107], v4 offset:41984
	ds_read_b128 v[108:111], v4 offset:44032
	ds_read_b128 v[112:115], v4 offset:46080
	ds_read_b128 v[116:119], v4 offset:48128
	s_waitcnt vmcnt(5)
	s_waitcnt lgkmcnt(0)
	s_barrier
	v_mfma_f32_16x16x32_bf16 v[120:123], v[72:75], v[88:91], v[120:123]
	s_add_u32 s33, s33, 0x8000
	s_cmp_eq_u32 s33, 0x18000
	s_cselect_b32 s33, 0, s33
	s_add_u32 s25, s25, 1
	s_mov_b32 m0, s26
	v_mfma_f32_16x16x32_bf16 v[124:127], v[76:79], v[88:91], v[124:127]
	buffer_load_dwordx4 v2, s[12:15], s44 offen sc1 lds
	v_mfma_f32_16x16x32_bf16 v[128:131], v[80:83], v[88:91], v[128:131]
	v_mfma_f32_16x16x32_bf16 v[132:135], v[84:87], v[88:91], v[132:135]
	v_mfma_f32_16x16x32_bf16 v[136:139], v[72:75], v[92:95], v[136:139]
	v_mfma_f32_16x16x32_bf16 v[140:143], v[76:79], v[92:95], v[140:143]
	s_add_u32 s42, s41, 0x10000
	buffer_load_dwordx4 v[24:27], v1, s[4:7], s42 offen sc0 nt
	v_mfma_f32_16x16x32_bf16 v[144:147], v[80:83], v[92:95], v[144:147]
	v_mfma_f32_16x16x32_bf16 v[148:151], v[84:87], v[92:95], v[148:151]
	v_mfma_f32_16x16x32_bf16 v[152:155], v[72:75], v[96:99], v[152:155]
	v_mfma_f32_16x16x32_bf16 v[156:159], v[76:79], v[96:99], v[156:159]
	buffer_load_dwordx4 v2, s[12:15], s44 offen offset:1024 sc1 lds
	v_mfma_f32_16x16x32_bf16 v[160:163], v[80:83], v[96:99], v[160:163]
	v_mfma_f32_16x16x32_bf16 v[164:167], v[84:87], v[96:99], v[164:167]
	v_mfma_f32_16x16x32_bf16 v[168:171], v[72:75], v[100:103], v[168:171]
	v_mfma_f32_16x16x32_bf16 v[172:175], v[76:79], v[100:103], v[172:175]
	s_add_u32 s42, s41, 0x14000
	buffer_load_dwordx4 v[28:31], v1, s[4:7], s42 offen sc0 nt
	v_mfma_f32_16x16x32_bf16 v[176:179], v[80:83], v[100:103], v[176:179]
	v_mfma_f32_16x16x32_bf16 v[180:183], v[84:87], v[100:103], v[180:183]
	v_mfma_f32_16x16x32_bf16 v[184:187], v[72:75], v[104:107], v[184:187]
	v_mfma_f32_16x16x32_bf16 v[188:191], v[76:79], v[104:107], v[188:191]
	buffer_load_dwordx4 v2, s[12:15], s44 offen offset:2048 sc1 lds
	v_mfma_f32_16x16x32_bf16 v[192:195], v[80:83], v[104:107], v[192:195]
	v_mfma_f32_16x16x32_bf16 v[196:199], v[84:87], v[104:107], v[196:199]
	v_mfma_f32_16x16x32_bf16 v[200:203], v[72:75], v[108:111], v[200:203]
	v_mfma_f32_16x16x32_bf16 v[204:207], v[76:79], v[108:111], v[204:207]
	s_add_u32 s42, s41, 0x18000
	buffer_load_dwordx4 v[32:35], v1, s[4:7], s42 offen sc0 nt
	v_mfma_f32_16x16x32_bf16 v[208:211], v[80:83], v[108:111], v[208:211]
	v_mfma_f32_16x16x32_bf16 v[212:215], v[84:87], v[108:111], v[212:215]
	v_mfma_f32_16x16x32_bf16 v[216:219], v[72:75], v[112:115], v[216:219]
	v_mfma_f32_16x16x32_bf16 v[220:223], v[76:79], v[112:115], v[220:223]
	buffer_load_dwordx4 v2, s[12:15], s44 offen offset:3072 sc1 lds
	v_mfma_f32_16x16x32_bf16 v[224:227], v[80:83], v[112:115], v[224:227]
	v_mfma_f32_16x16x32_bf16 v[228:231], v[84:87], v[112:115], v[228:231]
	v_mfma_f32_16x16x32_bf16 v[232:235], v[72:75], v[116:119], v[232:235]
	v_mfma_f32_16x16x32_bf16 v[236:239], v[76:79], v[116:119], v[236:239]
	s_add_u32 s42, s41, 0x1c000
	buffer_load_dwordx4 v[36:39], v1, s[4:7], s42 offen sc0 nt
	v_mfma_f32_16x16x32_bf16 v[240:243], v[80:83], v[116:119], v[240:243]
	s_add_u32 s26, s26, 0x8000
	s_cmp_eq_u32 s26, s32
	s_cselect_b32 s26, s27, s26
	v_mfma_f32_16x16x32_bf16 v[244:247], v[84:87], v[116:119], v[244:247]
	s_barrier
	s_mov_b32 s38, 4
.Lg_loop1:
	v_add_u32_e32 v6, s33, v5
	ds_read_b128 v[72:75], v6 offset:0
	ds_read_b128 v[76:79], v6 offset:2048
	ds_read_b128 v[80:83], v6 offset:4096
	ds_read_b128 v[84:87], v6 offset:6144
	ds_read_b128 v[88:91], v4 offset:0
	ds_read_b128 v[92:95], v4 offset:2048
	ds_read_b128 v[96:99], v4 offset:4096
	ds_read_b128 v[100:103], v4 offset:6144
	ds_read_b128 v[104:107], v4 offset:8192
	ds_read_b128 v[108:111], v4 offset:10240
	ds_read_b128 v[112:115], v4 offset:12288
	ds_read_b128 v[116:119], v4 offset:14336
	s_waitcnt vmcnt(22)
	v_cvt_pk_bf16_f32 v40, v40, v41
	v_cvt_pk_bf16_f32 v41, v42, v43
	v_cvt_pk_bf16_f32 v44, v44, v45
	v_cvt_pk_bf16_f32 v45, v46, v47
	ds_write2st64_b64 v3, v[40:41], v[44:45] offset0:64 offset1:72
	s_waitcnt vmcnt(20)
	v_cvt_pk_bf16_f32 v48, v48, v49
	v_cvt_pk_bf16_f32 v49, v50, v51
	v_cvt_pk_bf16_f32 v52, v52, v53
	v_cvt_pk_bf16_f32 v53, v54, v55
	ds_write2st64_b64 v3, v[48:49], v[52:53] offset0:80 offset1:88
	s_waitcnt vmcnt(16)
	v_cvt_pk_bf16_f32 v56, v56, v57
	v_cvt_pk_bf16_f32 v57, v58, v59
	v_cvt_pk_bf16_f32 v60, v60, v61
	v_cvt_pk_bf16_f32 v61, v62, v63
	ds_write2st64_b64 v3, v[56:57], v[60:61] offset0:96 offset1:104
	s_waitcnt vmcnt(12)
	v_cvt_pk_bf16_f32 v64, v64, v65
	v_cvt_pk_bf16_f32 v65, v66, v67
	v_cvt_pk_bf16_f32 v68, v68, v69
	v_cvt_pk_bf16_f32 v69, v70, v71
	ds_write2st64_b64 v3, v[64:65], v[68:69] offset0:112 offset1:120
	s_waitcnt lgkmcnt(0)
	s_barrier
	v_mfma_f32_16x16x32_bf16 v[120:123], v[72:75], v[88:91], v[120:123]
	s_min_u32 s40, s25, 31
	s_bitcmp1_b32 s40, 4
	s_cselect_b32 s41, s23, s22
	s_lshl_b32 s42, s40, 23
	s_and_b32 s42, s42, 0x7000000
	s_or_b32 s41, s41, s42
	s_lshl_b32 s42, s40, 8
	s_and_b32 s42, s42, 0x100
	s_or_b32 s41, s41, s42
	s_sub_u32 s43, s25, 1
	s_min_u32 s43, s43, 31
	s_and_b32 s43, s43, 15
	s_lshl_b32 s43, s43, 15
	s_add_u32 s44, s43, s24
	v_mfma_f32_16x16x32_bf16 v[124:127], v[76:79], v[88:91], v[124:127]
	v_mfma_f32_16x16x32_bf16 v[128:131], v[80:83], v[88:91], v[128:131]
	v_mfma_f32_16x16x32_bf16 v[132:135], v[84:87], v[88:91], v[132:135]
	buffer_load_dwordx4 v[40:43], v1, s[4:7], s41 offen sc0 nt
	v_mfma_f32_16x16x32_bf16 v[136:139], v[72:75], v[92:95], v[136:139]
	v_mfma_f32_16x16x32_bf16 v[140:143], v[76:79], v[92:95], v[140:143]
	v_mfma_f32_16x16x32_bf16 v[144:147], v[80:83], v[92:95], v[144:147]
	v_mfma_f32_16x16x32_bf16 v[148:151], v[84:87], v[92:95], v[148:151]
	v_mfma_f32_16x16x32_bf16 v[152:155], v[72:75], v[96:99], v[152:155]
	v_mfma_f32_16x16x32_bf16 v[156:159], v[76:79], v[96:99], v[156:159]
	v_mfma_f32_16x16x32_bf16 v[160:163], v[80:83], v[96:99], v[160:163]
	v_mfma_f32_16x16x32_bf16 v[164:167], v[84:87], v[96:99], v[164:167]
	s_add_u32 s42, s41, 0x4000
	buffer_load_dwordx4 v[44:47], v1, s[4:7], s42 offen sc0 nt
	v_mfma_f32_16x16x32_bf16 v[168:171], v[72:75], v[100:103], v[168:171]
	v_mfma_f32_16x16x32_bf16 v[172:175], v[76:79], v[100:103], v[172:175]
	v_mfma_f32_16x16x32_bf16 v[176:179], v[80:83], v[100:103], v[176:179]
	v_mfma_f32_16x16x32_bf16 v[180:183], v[84:87], v[100:103], v[180:183]
	v_mfma_f32_16x16x32_bf16 v[184:187], v[72:75], v[104:107], v[184:187]
	v_mfma_f32_16x16x32_bf16 v[188:191], v[76:79], v[104:107], v[188:191]
	v_mfma_f32_16x16x32_bf16 v[192:195], v[80:83], v[104:107], v[192:195]
	v_mfma_f32_16x16x32_bf16 v[196:199], v[84:87], v[104:107], v[196:199]
	s_add_u32 s42, s41, 0x8000
	buffer_load_dwordx4 v[48:51], v1, s[4:7], s42 offen sc0 nt
	v_mfma_f32_16x16x32_bf16 v[200:203], v[72:75], v[108:111], v[200:203]
	v_mfma_f32_16x16x32_bf16 v[204:207], v[76:79], v[108:111], v[204:207]
	v_mfma_f32_16x16x32_bf16 v[208:211], v[80:83], v[108:111], v[208:211]
	v_mfma_f32_16x16x32_bf16 v[212:215], v[84:87], v[108:111], v[212:215]
	v_mfma_f32_16x16x32_bf16 v[216:219], v[72:75], v[112:115], v[216:219]
	v_mfma_f32_16x16x32_bf16 v[220:223], v[76:79], v[112:115], v[220:223]
	v_mfma_f32_16x16x32_bf16 v[224:227], v[80:83], v[112:115], v[224:227]
	v_mfma_f32_16x16x32_bf16 v[228:231], v[84:87], v[112:115], v[228:231]
	s_add_u32 s42, s41, 0xc000
	buffer_load_dwordx4 v[52:55], v1, s[4:7], s42 offen sc0 nt
	v_mfma_f32_16x16x32_bf16 v[232:235], v[72:75], v[116:119], v[232:235]
	v_mfma_f32_16x16x32_bf16 v[236:239], v[76:79], v[116:119], v[236:239]
	v_mfma_f32_16x16x32_bf16 v[240:243], v[80:83], v[116:119], v[240:243]
	v_mfma_f32_16x16x32_bf16 v[244:247], v[84:87], v[116:119], v[244:247]
	s_barrier
	ds_read_b128 v[72:75], v6 offset:1024
	ds_read_b128 v[76:79], v6 offset:3072
	ds_read_b128 v[80:83], v6 offset:5120
	ds_read_b128 v[84:87], v6 offset:7168
	ds_read_b128 v[88:91], v4 offset:1024
	ds_read_b128 v[92:95], v4 offset:3072
	ds_read_b128 v[96:99], v4 offset:5120
	ds_read_b128 v[100:103], v4 offset:7168
	ds_read_b128 v[104:107], v4 offset:9216
	ds_read_b128 v[108:111], v4 offset:11264
	ds_read_b128 v[112:115], v4 offset:13312
	ds_read_b128 v[116:119], v4 offset:15360
	s_waitcnt vmcnt(5)
	s_waitcnt lgkmcnt(0)
	s_barrier
	v_mfma_f32_16x16x32_bf16 v[120:123], v[72:75], v[88:91], v[120:123]
	s_add_u32 s33, s33, 0x8000
	s_cmp_eq_u32 s33, 0x18000
	s_cselect_b32 s33, 0, s33
	s_add_u32 s25, s25, 1
	s_mov_b32 m0, s26
	v_mfma_f32_16x16x32_bf16 v[124:127], v[76:79], v[88:91], v[124:127]
	buffer_load_dwordx4 v2, s[12:15], s44 offen sc1 lds
	v_mfma_f32_16x16x32_bf16 v[128:131], v[80:83], v[88:91], v[128:131]
	v_mfma_f32_16x16x32_bf16 v[132:135], v[84:87], v[88:91], v[132:135]
	v_mfma_f32_16x16x32_bf16 v[136:139], v[72:75], v[92:95], v[136:139]
	v_mfma_f32_16x16x32_bf16 v[140:143], v[76:79], v[92:95], v[140:143]
	s_add_u32 s42, s41, 0x10000
	buffer_load_dwordx4 v[56:59], v1, s[4:7], s42 offen sc0 nt
	v_mfma_f32_16x16x32_bf16 v[144:147], v[80:83], v[92:95], v[144:147]
	v_mfma_f32_16x16x32_bf16 v[148:151], v[84:87], v[92:95], v[148:151]
	v_mfma_f32_16x16x32_bf16 v[152:155], v[72:75], v[96:99], v[152:155]
	v_mfma_f32_16x16x32_bf16 v[156:159], v[76:79], v[96:99], v[156:159]
	buffer_load_dwordx4 v2, s[12:15], s44 offen offset:1024 sc1 lds
	v_mfma_f32_16x16x32_bf16 v[160:163], v[80:83], v[96:99], v[160:163]
	v_mfma_f32_16x16x32_bf16 v[164:167], v[84:87], v[96:99], v[164:167]
	v_mfma_f32_16x16x32_bf16 v[168:171], v[72:75], v[100:103], v[168:171]
	v_mfma_f32_16x16x32_bf16 v[172:175], v[76:79], v[100:103], v[172:175]
	s_add_u32 s42, s41, 0x14000
	buffer_load_dwordx4 v[60:63], v1, s[4:7], s42 offen sc0 nt
	v_mfma_f32_16x16x32_bf16 v[176:179], v[80:83], v[100:103], v[176:179]
	v_mfma_f32_16x16x32_bf16 v[180:183], v[84:87], v[100:103], v[180:183]
	v_mfma_f32_16x16x32_bf16 v[184:187], v[72:75], v[104:107], v[184:187]
	v_mfma_f32_16x16x32_bf16 v[188:191], v[76:79], v[104:107], v[188:191]
	buffer_load_dwordx4 v2, s[12:15], s44 offen offset:2048 sc1 lds
	v_mfma_f32_16x16x32_bf16 v[192:195], v[80:83], v[104:107], v[192:195]
	v_mfma_f32_16x16x32_bf16 v[196:199], v[84:87], v[104:107], v[196:199]
	v_mfma_f32_16x16x32_bf16 v[200:203], v[72:75], v[108:111], v[200:203]
	v_mfma_f32_16x16x32_bf16 v[204:207], v[76:79], v[108:111], v[204:207]
	s_add_u32 s42, s41, 0x18000
	buffer_load_dwordx4 v[64:67], v1, s[4:7], s42 offen sc0 nt
	v_mfma_f32_16x16x32_bf16 v[208:211], v[80:83], v[108:111], v[208:211]
	v_mfma_f32_16x16x32_bf16 v[212:215], v[84:87], v[108:111], v[212:215]
	v_mfma_f32_16x16x32_bf16 v[216:219], v[72:75], v[112:115], v[216:219]
	v_mfma_f32_16x16x32_bf16 v[220:223], v[76:79], v[112:115], v[220:223]
	buffer_load_dwordx4 v2, s[12:15], s44 offen offset:3072 sc1 lds
	v_mfma_f32_16x16x32_bf16 v[224:227], v[80:83], v[112:115], v[224:227]
	v_mfma_f32_16x16x32_bf16 v[228:231], v[84:87], v[112:115], v[228:231]
	v_mfma_f32_16x16x32_bf16 v[232:235], v[72:75], v[116:119], v[232:235]
	v_mfma_f32_16x16x32_bf16 v[236:239], v[76:79], v[116:119], v[236:239]
	s_add_u32 s42, s41, 0x1c000
	buffer_load_dwordx4 v[68:71], v1, s[4:7], s42 offen sc0 nt
	v_mfma_f32_16x16x32_bf16 v[240:243], v[80:83], v[116:119], v[240:243]
	s_add_u32 s26, s26, 0x8000
	s_cmp_eq_u32 s26, s32
	s_cselect_b32 s26, s27, s26
	v_mfma_f32_16x16x32_bf16 v[244:247], v[84:87], v[116:119], v[244:247]
	s_barrier
	v_add_u32_e32 v6, s33, v5
	ds_read_b128 v[72:75], v6 offset:0
	ds_read_b128 v[76:79], v6 offset:2048
	ds_read_b128 v[80:83], v6 offset:4096
	ds_read_b128 v[84:87], v6 offset:6144
	ds_read_b128 v[88:91], v4 offset:32768
	ds_read_b128 v[92:95], v4 offset:34816
	ds_read_b128 v[96:99], v4 offset:36864
	ds_read_b128 v[100:103], v4 offset:38912
	ds_read_b128 v[104:107], v4 offset:40960
	ds_read_b128 v[108:111], v4 offset:43008
	ds_read_b128 v[112:115], v4 offset:45056
	ds_read_b128 v[116:119], v4 offset:47104
	s_waitcnt vmcnt(22)
	v_cvt_pk_bf16_f32 v8, v8, v9
	v_cvt_pk_bf16_f32 v9, v10, v11
	v_cvt_pk_bf16_f32 v12, v12, v13
	v_cvt_pk_bf16_f32 v13, v14, v15
	ds_write2st64_b64 v3, v[8:9], v[12:13] offset0:0 offset1:8
	s_waitcnt vmcnt(20)
	v_cvt_pk_bf16_f32 v16, v16, v17
	v_cvt_pk_bf16_f32 v17, v18, v19
	v_cvt_pk_bf16_f32 v20, v20, v21
	v_cvt_pk_bf16_f32 v21, v22, v23
	ds_write2st64_b64 v3, v[16:17], v[20:21] offset0:16 offset1:24
	s_waitcnt vmcnt(16)
	v_cvt_pk_bf16_f32 v24, v24, v25
	v_cvt_pk_bf16_f32 v25, v26, v27
	v_cvt_pk_bf16_f32 v28, v28, v29
	v_cvt_pk_bf16_f32 v29, v30, v31
	ds_write2st64_b64 v3, v[24:25], v[28:29] offset0:32 offset1:40
	s_waitcnt vmcnt(12)
	v_cvt_pk_bf16_f32 v32, v32, v33
	v_cvt_pk_bf16_f32 v33, v34, v35
	v_cvt_pk_bf16_f32 v36, v36, v37
	v_cvt_pk_bf16_f32 v37, v38, v39
	ds_write2st64_b64 v3, v[32:33], v[36:37] offset0:48 offset1:56
	s_waitcnt lgkmcnt(0)
	s_barrier
	v_mfma_f32_16x16x32_bf16 v[120:123], v[72:75], v[88:91], v[120:123]
	s_min_u32 s40, s25, 31
	s_bitcmp1_b32 s40, 4
	s_cselect_b32 s41, s23, s22
	s_lshl_b32 s42, s40, 23
	s_and_b32 s42, s42, 0x7000000
	s_or_b32 s41, s41, s42
	s_lshl_b32 s42, s40, 8
	s_and_b32 s42, s42, 0x100
	s_or_b32 s41, s41, s42
	s_sub_u32 s43, s25, 1
	s_min_u32 s43, s43, 31
	s_and_b32 s43, s43, 15
	s_lshl_b32 s43, s43, 15
	s_add_u32 s44, s43, s24
	v_mfma_f32_16x16x32_bf16 v[124:127], v[76:79], v[88:91], v[124:127]
	v_mfma_f32_16x16x32_bf16 v[128:131], v[80:83], v[88:91], v[128:131]
	v_mfma_f32_16x16x32_bf16 v[132:135], v[84:87], v[88:91], v[132:135]
	buffer_load_dwordx4 v[8:11], v1, s[4:7], s41 offen sc0 nt
	v_mfma_f32_16x16x32_bf16 v[136:139], v[72:75], v[92:95], v[136:139]
	v_mfma_f32_16x16x32_bf16 v[140:143], v[76:79], v[92:95], v[140:143]
	v_mfma_f32_16x16x32_bf16 v[144:147], v[80:83], v[92:95], v[144:147]
	v_mfma_f32_16x16x32_bf16 v[148:151], v[84:87], v[92:95], v[148:151]
	v_mfma_f32_16x16x32_bf16 v[152:155], v[72:75], v[96:99], v[152:155]
	v_mfma_f32_16x16x32_bf16 v[156:159], v[76:79], v[96:99], v[156:159]
	v_mfma_f32_16x16x32_bf16 v[160:163], v[80:83], v[96:99], v[160:163]
	v_mfma_f32_16x16x32_bf16 v[164:167], v[84:87], v[96:99], v[164:167]
	s_add_u32 s42, s41, 0x4000
	buffer_load_dwordx4 v[12:15], v1, s[4:7], s42 offen sc0 nt
	v_mfma_f32_16x16x32_bf16 v[168:171], v[72:75], v[100:103], v[168:171]
	v_mfma_f32_16x16x32_bf16 v[172:175], v[76:79], v[100:103], v[172:175]
	v_mfma_f32_16x16x32_bf16 v[176:179], v[80:83], v[100:103], v[176:179]
	v_mfma_f32_16x16x32_bf16 v[180:183], v[84:87], v[100:103], v[180:183]
	v_mfma_f32_16x16x32_bf16 v[184:187], v[72:75], v[104:107], v[184:187]
	v_mfma_f32_16x16x32_bf16 v[188:191], v[76:79], v[104:107], v[188:191]
	v_mfma_f32_16x16x32_bf16 v[192:195], v[80:83], v[104:107], v[192:195]
	v_mfma_f32_16x16x32_bf16 v[196:199], v[84:87], v[104:107], v[196:199]
	s_add_u32 s42, s41, 0x8000
	buffer_load_dwordx4 v[16:19], v1, s[4:7], s42 offen sc0 nt
	v_mfma_f32_16x16x32_bf16 v[200:203], v[72:75], v[108:111], v[200:203]
	v_mfma_f32_16x16x32_bf16 v[204:207], v[76:79], v[108:111], v[204:207]
	v_mfma_f32_16x16x32_bf16 v[208:211], v[80:83], v[108:111], v[208:211]
	v_mfma_f32_16x16x32_bf16 v[212:215], v[84:87], v[108:111], v[212:215]
	v_mfma_f32_16x16x32_bf16 v[216:219], v[72:75], v[112:115], v[216:219]
	v_mfma_f32_16x16x32_bf16 v[220:223], v[76:79], v[112:115], v[220:223]
	v_mfma_f32_16x16x32_bf16 v[224:227], v[80:83], v[112:115], v[224:227]
	v_mfma_f32_16x16x32_bf16 v[228:231], v[84:87], v[112:115], v[228:231]
	s_add_u32 s42, s41, 0xc000
	buffer_load_dwordx4 v[20:23], v1, s[4:7], s42 offen sc0 nt
	v_mfma_f32_16x16x32_bf16 v[232:235], v[72:75], v[116:119], v[232:235]
	v_mfma_f32_16x16x32_bf16 v[236:239], v[76:79], v[116:119], v[236:239]
	v_mfma_f32_16x16x32_bf16 v[240:243], v[80:83], v[116:119], v[240:243]
	v_mfma_f32_16x16x32_bf16 v[244:247], v[84:87], v[116:119], v[244:247]
	s_barrier
	ds_read_b128 v[72:75], v6 offset:1024
	ds_read_b128 v[76:79], v6 offset:3072
	ds_read_b128 v[80:83], v6 offset:5120
	ds_read_b128 v[84:87], v6 offset:7168
	ds_read_b128 v[88:91], v4 offset:33792
	ds_read_b128 v[92:95], v4 offset:35840
	ds_read_b128 v[96:99], v4 offset:37888
	ds_read_b128 v[100:103], v4 offset:39936
	ds_read_b128 v[104:107], v4 offset:41984
	ds_read_b128 v[108:111], v4 offset:44032
	ds_read_b128 v[112:115], v4 offset:46080
	ds_read_b128 v[116:119], v4 offset:48128
	s_waitcnt vmcnt(5)
	s_waitcnt lgkmcnt(0)
	s_barrier
	v_mfma_f32_16x16x32_bf16 v[120:123], v[72:75], v[88:91], v[120:123]
	s_add_u32 s33, s33, 0x8000
	s_cmp_eq_u32 s33, 0x18000
	s_cselect_b32 s33, 0, s33
	s_add_u32 s25, s25, 1
	s_mov_b32 m0, s26
	v_mfma_f32_16x16x32_bf16 v[124:127], v[76:79], v[88:91], v[124:127]
	buffer_load_dwordx4 v2, s[12:15], s44 offen sc1 lds
	v_mfma_f32_16x16x32_bf16 v[128:131], v[80:83], v[88:91], v[128:131]
	v_mfma_f32_16x16x32_bf16 v[132:135], v[84:87], v[88:91], v[132:135]
	v_mfma_f32_16x16x32_bf16 v[136:139], v[72:75], v[92:95], v[136:139]
	v_mfma_f32_16x16x32_bf16 v[140:143], v[76:79], v[92:95], v[140:143]
	s_add_u32 s42, s41, 0x10000
	buffer_load_dwordx4 v[24:27], v1, s[4:7], s42 offen sc0 nt
	v_mfma_f32_16x16x32_bf16 v[144:147], v[80:83], v[92:95], v[144:147]
	v_mfma_f32_16x16x32_bf16 v[148:151], v[84:87], v[92:95], v[148:151]
	v_mfma_f32_16x16x32_bf16 v[152:155], v[72:75], v[96:99], v[152:155]
	v_mfma_f32_16x16x32_bf16 v[156:159], v[76:79], v[96:99], v[156:159]
	buffer_load_dwordx4 v2, s[12:15], s44 offen offset:1024 sc1 lds
	v_mfma_f32_16x16x32_bf16 v[160:163], v[80:83], v[96:99], v[160:163]
	v_mfma_f32_16x16x32_bf16 v[164:167], v[84:87], v[96:99], v[164:167]
	v_mfma_f32_16x16x32_bf16 v[168:171], v[72:75], v[100:103], v[168:171]
	v_mfma_f32_16x16x32_bf16 v[172:175], v[76:79], v[100:103], v[172:175]
	s_add_u32 s42, s41, 0x14000
	buffer_load_dwordx4 v[28:31], v1, s[4:7], s42 offen sc0 nt
	v_mfma_f32_16x16x32_bf16 v[176:179], v[80:83], v[100:103], v[176:179]
	v_mfma_f32_16x16x32_bf16 v[180:183], v[84:87], v[100:103], v[180:183]
	v_mfma_f32_16x16x32_bf16 v[184:187], v[72:75], v[104:107], v[184:187]
	v_mfma_f32_16x16x32_bf16 v[188:191], v[76:79], v[104:107], v[188:191]
	buffer_load_dwordx4 v2, s[12:15], s44 offen offset:2048 sc1 lds
	v_mfma_f32_16x16x32_bf16 v[192:195], v[80:83], v[104:107], v[192:195]
	v_mfma_f32_16x16x32_bf16 v[196:199], v[84:87], v[104:107], v[196:199]
	v_mfma_f32_16x16x32_bf16 v[200:203], v[72:75], v[108:111], v[200:203]
	v_mfma_f32_16x16x32_bf16 v[204:207], v[76:79], v[108:111], v[204:207]
	s_add_u32 s42, s41, 0x18000
	buffer_load_dwordx4 v[32:35], v1, s[4:7], s42 offen sc0 nt
	v_mfma_f32_16x16x32_bf16 v[208:211], v[80:83], v[108:111], v[208:211]
	v_mfma_f32_16x16x32_bf16 v[212:215], v[84:87], v[108:111], v[212:215]
	v_mfma_f32_16x16x32_bf16 v[216:219], v[72:75], v[112:115], v[216:219]
	v_mfma_f32_16x16x32_bf16 v[220:223], v[76:79], v[112:115], v[220:223]
	buffer_load_dwordx4 v2, s[12:15], s44 offen offset:3072 sc1 lds
	v_mfma_f32_16x16x32_bf16 v[224:227], v[80:83], v[112:115], v[224:227]
	v_mfma_f32_16x16x32_bf16 v[228:231], v[84:87], v[112:115], v[228:231]
	v_mfma_f32_16x16x32_bf16 v[232:235], v[72:75], v[116:119], v[232:235]
	v_mfma_f32_16x16x32_bf16 v[236:239], v[76:79], v[116:119], v[236:239]
	s_add_u32 s42, s41, 0x1c000
	buffer_load_dwordx4 v[36:39], v1, s[4:7], s42 offen sc0 nt
	v_mfma_f32_16x16x32_bf16 v[240:243], v[80:83], v[116:119], v[240:243]
	s_add_u32 s26, s26, 0x8000
	s_cmp_eq_u32 s26, s32
	s_cselect_b32 s26, s27, s26
	v_mfma_f32_16x16x32_bf16 v[244:247], v[84:87], v[116:119], v[244:247]
	s_barrier
	s_sub_u32 s38, s38, 1
	s_cmp_lg_u32 s38, 0
	s_cbranch_scc1 .Lg_loop1
	v_add_u32_e32 v6, s33, v5
	ds_read_b128 v[72:75], v6 offset:0
	ds_read_b128 v[76:79], v6 offset:2048
	ds_read_b128 v[80:83], v6 offset:4096
	ds_read_b128 v[84:87], v6 offset:6144
	ds_read_b128 v[88:91], v4 offset:0
	ds_read_b128 v[92:95], v4 offset:2048
	ds_read_b128 v[96:99], v4 offset:4096
	ds_read_b128 v[100:103], v4 offset:6144
	ds_read_b128 v[104:107], v4 offset:8192
	ds_read_b128 v[108:111], v4 offset:10240
	ds_read_b128 v[112:115], v4 offset:12288
	ds_read_b128 v[116:119], v4 offset:14336
	s_waitcnt vmcnt(22)
	v_cvt_pk_bf16_f32 v40, v40, v41
	v_cvt_pk_bf16_f32 v41, v42, v43
	v_cvt_pk_bf16_f32 v44, v44, v45
	v_cvt_pk_bf16_f32 v45, v46, v47
	ds_write2st64_b64 v3, v[40:41], v[44:45] offset0:64 offset1:72
	s_waitcnt vmcnt(20)
	v_cvt_pk_bf16_f32 v48, v48, v49
	v_cvt_pk_bf16_f32 v49, v50, v51
	v_cvt_pk_bf16_f32 v52, v52, v53
	v_cvt_pk_bf16_f32 v53, v54, v55
	ds_write2st64_b64 v3, v[48:49], v[52:53] offset0:80 offset1:88
	s_waitcnt vmcnt(16)
	v_cvt_pk_bf16_f32 v56, v56, v57
	v_cvt_pk_bf16_f32 v57, v58, v59
	v_cvt_pk_bf16_f32 v60, v60, v61
	v_cvt_pk_bf16_f32 v61, v62, v63
	ds_write2st64_b64 v3, v[56:57], v[60:61] offset0:96 offset1:104
	s_waitcnt vmcnt(12)
	v_cvt_pk_bf16_f32 v64, v64, v65
	v_cvt_pk_bf16_f32 v65, v66, v67
	v_cvt_pk_bf16_f32 v68, v68, v69
	v_cvt_pk_bf16_f32 v69, v70, v71
	ds_write2st64_b64 v3, v[64:65], v[68:69] offset0:112 offset1:120
	s_waitcnt lgkmcnt(0)
	s_barrier
	v_mfma_f32_16x16x32_bf16 v[120:123], v[72:75], v[88:91], v[120:123]
	s_min_u32 s40, s25, 31
	s_bitcmp1_b32 s40, 4
	s_cselect_b32 s41, s23, s22
	s_lshl_b32 s42, s40, 23
	s_and_b32 s42, s42, 0x7000000
	s_or_b32 s41, s41, s42
	s_lshl_b32 s42, s40, 8
	s_and_b32 s42, s42, 0x100
	s_or_b32 s41, s41, s42
	s_sub_u32 s43, s25, 1
	s_min_u32 s43, s43, 31
	s_and_b32 s43, s43, 15
	s_lshl_b32 s43, s43, 15
	s_add_u32 s44, s43, s24
	v_mfma_f32_16x16x32_bf16 v[124:127], v[76:79], v[88:91], v[124:127]
	v_mfma_f32_16x16x32_bf16 v[128:131], v[80:83], v[88:91], v[128:131]
	v_mfma_f32_16x16x32_bf16 v[132:135], v[84:87], v[88:91], v[132:135]
	buffer_load_dwordx4 v[40:43], v1, s[4:7], s41 offen sc0 nt
	v_mfma_f32_16x16x32_bf16 v[136:139], v[72:75], v[92:95], v[136:139]
	v_mfma_f32_16x16x32_bf16 v[140:143], v[76:79], v[92:95], v[140:143]
	v_mfma_f32_16x16x32_bf16 v[144:147], v[80:83], v[92:95], v[144:147]
	v_mfma_f32_16x16x32_bf16 v[148:151], v[84:87], v[92:95], v[148:151]
	v_mfma_f32_16x16x32_bf16 v[152:155], v[72:75], v[96:99], v[152:155]
	v_mfma_f32_16x16x32_bf16 v[156:159], v[76:79], v[96:99], v[156:159]
	v_mfma_f32_16x16x32_bf16 v[160:163], v[80:83], v[96:99], v[160:163]
	v_mfma_f32_16x16x32_bf16 v[164:167], v[84:87], v[96:99], v[164:167]
	s_add_u32 s42, s41, 0x4000
	buffer_load_dwordx4 v[44:47], v1, s[4:7], s42 offen sc0 nt
	v_mfma_f32_16x16x32_bf16 v[168:171], v[72:75], v[100:103], v[168:171]
	v_mfma_f32_16x16x32_bf16 v[172:175], v[76:79], v[100:103], v[172:175]
	v_mfma_f32_16x16x32_bf16 v[176:179], v[80:83], v[100:103], v[176:179]
	v_mfma_f32_16x16x32_bf16 v[180:183], v[84:87], v[100:103], v[180:183]
	v_mfma_f32_16x16x32_bf16 v[184:187], v[72:75], v[104:107], v[184:187]
	v_mfma_f32_16x16x32_bf16 v[188:191], v[76:79], v[104:107], v[188:191]
	v_mfma_f32_16x16x32_bf16 v[192:195], v[80:83], v[104:107], v[192:195]
	v_mfma_f32_16x16x32_bf16 v[196:199], v[84:87], v[104:107], v[196:199]
	s_add_u32 s42, s41, 0x8000
	buffer_load_dwordx4 v[48:51], v1, s[4:7], s42 offen sc0 nt
	v_mfma_f32_16x16x32_bf16 v[200:203], v[72:75], v[108:111], v[200:203]
	v_mfma_f32_16x16x32_bf16 v[204:207], v[76:79], v[108:111], v[204:207]
	v_mfma_f32_16x16x32_bf16 v[208:211], v[80:83], v[108:111], v[208:211]
	v_mfma_f32_16x16x32_bf16 v[212:215], v[84:87], v[108:111], v[212:215]
	v_mfma_f32_16x16x32_bf16 v[216:219], v[72:75], v[112:115], v[216:219]
	v_mfma_f32_16x16x32_bf16 v[220:223], v[76:79], v[112:115], v[220:223]
	v_mfma_f32_16x16x32_bf16 v[224:227], v[80:83], v[112:115], v[224:227]
	v_mfma_f32_16x16x32_bf16 v[228:231], v[84:87], v[112:115], v[228:231]
	s_add_u32 s42, s41, 0xc000
	buffer_load_dwordx4 v[52:55], v1, s[4:7], s42 offen sc0 nt
	v_mfma_f32_16x16x32_bf16 v[232:235], v[72:75], v[116:119], v[232:235]
	v_mfma_f32_16x16x32_bf16 v[236:239], v[76:79], v[116:119], v[236:239]
	v_mfma_f32_16x16x32_bf16 v[240:243], v[80:83], v[116:119], v[240:243]
	v_mfma_f32_16x16x32_bf16 v[244:247], v[84:87], v[116:119], v[244:247]
	s_barrier
	ds_read_b128 v[72:75], v6 offset:1024
	ds_read_b128 v[76:79], v6 offset:3072
	ds_read_b128 v[80:83], v6 offset:5120
	ds_read_b128 v[84:87], v6 offset:7168
	ds_read_b128 v[88:91], v4 offset:1024
	ds_read_b128 v[92:95], v4 offset:3072
	ds_read_b128 v[96:99], v4 offset:5120
	ds_read_b128 v[100:103], v4 offset:7168
	ds_read_b128 v[104:107], v4 offset:9216
	ds_read_b128 v[108:111], v4 offset:11264
	ds_read_b128 v[112:115], v4 offset:13312
	ds_read_b128 v[116:119], v4 offset:15360
	s_waitcnt vmcnt(5)
	s_waitcnt lgkmcnt(0)
	s_barrier
	v_mfma_f32_16x16x32_bf16 v[120:123], v[72:75], v[88:91], v[120:123]
	s_add_u32 s33, s33, 0x8000
	s_cmp_eq_u32 s33, 0x18000
	s_cselect_b32 s33, 0, s33
	s_add_u32 s25, s25, 1
	s_mov_b32 m0, s26
	v_mfma_f32_16x16x32_bf16 v[124:127], v[76:79], v[88:91], v[124:127]
	buffer_load_dwordx4 v2, s[12:15], s44 offen sc1 lds
	v_mfma_f32_16x16x32_bf16 v[128:131], v[80:83], v[88:91], v[128:131]
	v_mfma_f32_16x16x32_bf16 v[132:135], v[84:87], v[88:91], v[132:135]
	v_mfma_f32_16x16x32_bf16 v[136:139], v[72:75], v[92:95], v[136:139]
	v_mfma_f32_16x16x32_bf16 v[140:143], v[76:79], v[92:95], v[140:143]
	s_add_u32 s42, s41, 0x10000
	buffer_load_dwordx4 v[56:59], v1, s[4:7], s42 offen sc0 nt
	v_mfma_f32_16x16x32_bf16 v[144:147], v[80:83], v[92:95], v[144:147]
	v_mfma_f32_16x16x32_bf16 v[148:151], v[84:87], v[92:95], v[148:151]
	v_mfma_f32_16x16x32_bf16 v[152:155], v[72:75], v[96:99], v[152:155]
	v_mfma_f32_16x16x32_bf16 v[156:159], v[76:79], v[96:99], v[156:159]
	buffer_load_dwordx4 v2, s[12:15], s44 offen offset:1024 sc1 lds
	v_mfma_f32_16x16x32_bf16 v[160:163], v[80:83], v[96:99], v[160:163]
	v_mfma_f32_16x16x32_bf16 v[164:167], v[84:87], v[96:99], v[164:167]
	v_mfma_f32_16x16x32_bf16 v[168:171], v[72:75], v[100:103], v[168:171]
	v_mfma_f32_16x16x32_bf16 v[172:175], v[76:79], v[100:103], v[172:175]
	s_add_u32 s42, s41, 0x14000
	buffer_load_dwordx4 v[60:63], v1, s[4:7], s42 offen sc0 nt
	v_mfma_f32_16x16x32_bf16 v[176:179], v[80:83], v[100:103], v[176:179]
	v_mfma_f32_16x16x32_bf16 v[180:183], v[84:87], v[100:103], v[180:183]
	v_mfma_f32_16x16x32_bf16 v[184:187], v[72:75], v[104:107], v[184:187]
	v_mfma_f32_16x16x32_bf16 v[188:191], v[76:79], v[104:107], v[188:191]
	buffer_load_dwordx4 v2, s[12:15], s44 offen offset:2048 sc1 lds
	v_mfma_f32_16x16x32_bf16 v[192:195], v[80:83], v[104:107], v[192:195]
	v_mfma_f32_16x16x32_bf16 v[196:199], v[84:87], v[104:107], v[196:199]
	v_mfma_f32_16x16x32_bf16 v[200:203], v[72:75], v[108:111], v[200:203]
	v_mfma_f32_16x16x32_bf16 v[204:207], v[76:79], v[108:111], v[204:207]
	s_add_u32 s42, s41, 0x18000
	buffer_load_dwordx4 v[64:67], v1, s[4:7], s42 offen sc0 nt
	v_mfma_f32_16x16x32_bf16 v[208:211], v[80:83], v[108:111], v[208:211]
	v_mfma_f32_16x16x32_bf16 v[212:215], v[84:87], v[108:111], v[212:215]
	v_mfma_f32_16x16x32_bf16 v[216:219], v[72:75], v[112:115], v[216:219]
	v_mfma_f32_16x16x32_bf16 v[220:223], v[76:79], v[112:115], v[220:223]
	buffer_load_dwordx4 v2, s[12:15], s44 offen offset:3072 sc1 lds
	v_mfma_f32_16x16x32_bf16 v[224:227], v[80:83], v[112:115], v[224:227]
	v_mfma_f32_16x16x32_bf16 v[228:231], v[84:87], v[112:115], v[228:231]
	v_mfma_f32_16x16x32_bf16 v[232:235], v[72:75], v[116:119], v[232:235]
	v_mfma_f32_16x16x32_bf16 v[236:239], v[76:79], v[116:119], v[236:239]
	s_add_u32 s42, s41, 0x1c000
	buffer_load_dwordx4 v[68:71], v1, s[4:7], s42 offen sc0 nt
	v_mfma_f32_16x16x32_bf16 v[240:243], v[80:83], v[116:119], v[240:243]
	s_add_u32 s26, s26, 0x8000
	s_cmp_eq_u32 s26, s32
	s_cselect_b32 s26, s27, s26
	v_mfma_f32_16x16x32_bf16 v[244:247], v[84:87], v[116:119], v[244:247]
	s_barrier
	v_add_u32_e32 v6, s33, v5
	ds_read_b128 v[72:75], v6 offset:0
	ds_read_b128 v[76:79], v6 offset:2048
	ds_read_b128 v[80:83], v6 offset:4096
	ds_read_b128 v[84:87], v6 offset:6144
	ds_read_b128 v[88:91], v4 offset:32768
	ds_read_b128 v[92:95], v4 offset:34816
	ds_read_b128 v[96:99], v4 offset:36864
	ds_read_b128 v[100:103], v4 offset:38912
	ds_read_b128 v[104:107], v4 offset:40960
	ds_read_b128 v[108:111], v4 offset:43008
	ds_read_b128 v[112:115], v4 offset:45056
	ds_read_b128 v[116:119], v4 offset:47104
	s_waitcnt vmcnt(22)
	v_cvt_pk_bf16_f32 v8, v8, v9
	v_cvt_pk_bf16_f32 v9, v10, v11
	v_cvt_pk_bf16_f32 v12, v12, v13
	v_cvt_pk_bf16_f32 v13, v14, v15
	ds_write2st64_b64 v3, v[8:9], v[12:13] offset0:0 offset1:8
	s_waitcnt vmcnt(20)
	v_cvt_pk_bf16_f32 v16, v16, v17
	v_cvt_pk_bf16_f32 v17, v18, v19
	v_cvt_pk_bf16_f32 v20, v20, v21
	v_cvt_pk_bf16_f32 v21, v22, v23
	ds_write2st64_b64 v3, v[16:17], v[20:21] offset0:16 offset1:24
	s_waitcnt vmcnt(16)
	v_cvt_pk_bf16_f32 v24, v24, v25
	v_cvt_pk_bf16_f32 v25, v26, v27
	v_cvt_pk_bf16_f32 v28, v28, v29
	v_cvt_pk_bf16_f32 v29, v30, v31
	ds_write2st64_b64 v3, v[24:25], v[28:29] offset0:32 offset1:40
	s_waitcnt vmcnt(12)
	v_cvt_pk_bf16_f32 v32, v32, v33
	v_cvt_pk_bf16_f32 v33, v34, v35
	v_cvt_pk_bf16_f32 v36, v36, v37
	v_cvt_pk_bf16_f32 v37, v38, v39
	ds_write2st64_b64 v3, v[32:33], v[36:37] offset0:48 offset1:56
	s_waitcnt lgkmcnt(0)
	s_barrier
	v_mfma_f32_16x16x32_bf16 v[120:123], v[72:75], v[88:91], v[120:123]
	s_min_u32 s40, s25, 31
	s_bitcmp1_b32 s40, 4
	s_cselect_b32 s41, s23, s22
	s_lshl_b32 s42, s40, 23
	s_and_b32 s42, s42, 0x7000000
	s_or_b32 s41, s41, s42
	s_lshl_b32 s42, s40, 8
	s_and_b32 s42, s42, 0x100
	s_or_b32 s41, s41, s42
	s_sub_u32 s43, s25, 1
	s_min_u32 s43, s43, 31
	s_and_b32 s43, s43, 15
	s_lshl_b32 s43, s43, 15
	s_add_u32 s44, s43, s24
	v_mfma_f32_16x16x32_bf16 v[124:127], v[76:79], v[88:91], v[124:127]
	v_mfma_f32_16x16x32_bf16 v[128:131], v[80:83], v[88:91], v[128:131]
	v_mfma_f32_16x16x32_bf16 v[132:135], v[84:87], v[88:91], v[132:135]
	v_mfma_f32_16x16x32_bf16 v[136:139], v[72:75], v[92:95], v[136:139]
	v_mfma_f32_16x16x32_bf16 v[140:143], v[76:79], v[92:95], v[140:143]
	v_mfma_f32_16x16x32_bf16 v[144:147], v[80:83], v[92:95], v[144:147]
	v_mfma_f32_16x16x32_bf16 v[148:151], v[84:87], v[92:95], v[148:151]
	v_mfma_f32_16x16x32_bf16 v[152:155], v[72:75], v[96:99], v[152:155]
	v_mfma_f32_16x16x32_bf16 v[156:159], v[76:79], v[96:99], v[156:159]
	v_mfma_f32_16x16x32_bf16 v[160:163], v[80:83], v[96:99], v[160:163]
	v_mfma_f32_16x16x32_bf16 v[164:167], v[84:87], v[96:99], v[164:167]
	v_mfma_f32_16x16x32_bf16 v[168:171], v[72:75], v[100:103], v[168:171]
	v_mfma_f32_16x16x32_bf16 v[172:175], v[76:79], v[100:103], v[172:175]
	v_mfma_f32_16x16x32_bf16 v[176:179], v[80:83], v[100:103], v[176:179]
	v_mfma_f32_16x16x32_bf16 v[180:183], v[84:87], v[100:103], v[180:183]
	v_mfma_f32_16x16x32_bf16 v[184:187], v[72:75], v[104:107], v[184:187]
	v_mfma_f32_16x16x32_bf16 v[188:191], v[76:79], v[104:107], v[188:191]
	v_mfma_f32_16x16x32_bf16 v[192:195], v[80:83], v[104:107], v[192:195]
	v_mfma_f32_16x16x32_bf16 v[196:199], v[84:87], v[104:107], v[196:199]
	v_mfma_f32_16x16x32_bf16 v[200:203], v[72:75], v[108:111], v[200:203]
	v_mfma_f32_16x16x32_bf16 v[204:207], v[76:79], v[108:111], v[204:207]
	v_mfma_f32_16x16x32_bf16 v[208:211], v[80:83], v[108:111], v[208:211]
	v_mfma_f32_16x16x32_bf16 v[212:215], v[84:87], v[108:111], v[212:215]
	v_mfma_f32_16x16x32_bf16 v[216:219], v[72:75], v[112:115], v[216:219]
	v_mfma_f32_16x16x32_bf16 v[220:223], v[76:79], v[112:115], v[220:223]
	v_mfma_f32_16x16x32_bf16 v[224:227], v[80:83], v[112:115], v[224:227]
	v_mfma_f32_16x16x32_bf16 v[228:231], v[84:87], v[112:115], v[228:231]
	v_mfma_f32_16x16x32_bf16 v[232:235], v[72:75], v[116:119], v[232:235]
	v_mfma_f32_16x16x32_bf16 v[236:239], v[76:79], v[116:119], v[236:239]
	v_mfma_f32_16x16x32_bf16 v[240:243], v[80:83], v[116:119], v[240:243]
	v_mfma_f32_16x16x32_bf16 v[244:247], v[84:87], v[116:119], v[244:247]
	s_barrier
	ds_read_b128 v[72:75], v6 offset:1024
	ds_read_b128 v[76:79], v6 offset:3072
	ds_read_b128 v[80:83], v6 offset:5120
	ds_read_b128 v[84:87], v6 offset:7168
	ds_read_b128 v[88:91], v4 offset:33792
	ds_read_b128 v[92:95], v4 offset:35840
	ds_read_b128 v[96:99], v4 offset:37888
	ds_read_b128 v[100:103], v4 offset:39936
	ds_read_b128 v[104:107], v4 offset:41984
	ds_read_b128 v[108:111], v4 offset:44032
	ds_read_b128 v[112:115], v4 offset:46080
	ds_read_b128 v[116:119], v4 offset:48128
	s_waitcnt vmcnt(1)
	s_waitcnt lgkmcnt(0)
	s_barrier
	v_mfma_f32_16x16x32_bf16 v[120:123], v[72:75], v[88:91], v[120:123]
	s_add_u32 s33, s33, 0x8000
	s_cmp_eq_u32 s33, 0x18000
	s_cselect_b32 s33, 0, s33
	s_add_u32 s25, s25, 1
	s_mov_b32 m0, s26
	v_mfma_f32_16x16x32_bf16 v[124:127], v[76:79], v[88:91], v[124:127]
	buffer_load_dwordx4 v2, s[12:15], s44 offen sc1 lds
	v_mfma_f32_16x16x32_bf16 v[128:131], v[80:83], v[88:91], v[128:131]
	v_mfma_f32_16x16x32_bf16 v[132:135], v[84:87], v[88:91], v[132:135]
	v_mfma_f32_16x16x32_bf16 v[136:139], v[72:75], v[92:95], v[136:139]
	v_mfma_f32_16x16x32_bf16 v[140:143], v[76:79], v[92:95], v[140:143]
	v_mfma_f32_16x16x32_bf16 v[144:147], v[80:83], v[92:95], v[144:147]
	v_mfma_f32_16x16x32_bf16 v[148:151], v[84:87], v[92:95], v[148:151]
	v_mfma_f32_16x16x32_bf16 v[152:155], v[72:75], v[96:99], v[152:155]
	v_mfma_f32_16x16x32_bf16 v[156:159], v[76:79], v[96:99], v[156:159]
	buffer_load_dwordx4 v2, s[12:15], s44 offen offset:1024 sc1 lds
	v_mfma_f32_16x16x32_bf16 v[160:163], v[80:83], v[96:99], v[160:163]
	v_mfma_f32_16x16x32_bf16 v[164:167], v[84:87], v[96:99], v[164:167]
	v_mfma_f32_16x16x32_bf16 v[168:171], v[72:75], v[100:103], v[168:171]
	v_mfma_f32_16x16x32_bf16 v[172:175], v[76:79], v[100:103], v[172:175]
	v_mfma_f32_16x16x32_bf16 v[176:179], v[80:83], v[100:103], v[176:179]
	v_mfma_f32_16x16x32_bf16 v[180:183], v[84:87], v[100:103], v[180:183]
	v_mfma_f32_16x16x32_bf16 v[184:187], v[72:75], v[104:107], v[184:187]
	v_mfma_f32_16x16x32_bf16 v[188:191], v[76:79], v[104:107], v[188:191]
	buffer_load_dwordx4 v2, s[12:15], s44 offen offset:2048 sc1 lds
	v_mfma_f32_16x16x32_bf16 v[192:195], v[80:83], v[104:107], v[192:195]
	v_mfma_f32_16x16x32_bf16 v[196:199], v[84:87], v[104:107], v[196:199]
	v_mfma_f32_16x16x32_bf16 v[200:203], v[72:75], v[108:111], v[200:203]
	v_mfma_f32_16x16x32_bf16 v[204:207], v[76:79], v[108:111], v[204:207]
	v_mfma_f32_16x16x32_bf16 v[208:211], v[80:83], v[108:111], v[208:211]
	v_mfma_f32_16x16x32_bf16 v[212:215], v[84:87], v[108:111], v[212:215]
	v_mfma_f32_16x16x32_bf16 v[216:219], v[72:75], v[112:115], v[216:219]
	v_mfma_f32_16x16x32_bf16 v[220:223], v[76:79], v[112:115], v[220:223]
	buffer_load_dwordx4 v2, s[12:15], s44 offen offset:3072 sc1 lds
	v_mfma_f32_16x16x32_bf16 v[224:227], v[80:83], v[112:115], v[224:227]
	v_mfma_f32_16x16x32_bf16 v[228:231], v[84:87], v[112:115], v[228:231]
	v_mfma_f32_16x16x32_bf16 v[232:235], v[72:75], v[116:119], v[232:235]
	v_mfma_f32_16x16x32_bf16 v[236:239], v[76:79], v[116:119], v[236:239]
	v_mfma_f32_16x16x32_bf16 v[240:243], v[80:83], v[116:119], v[240:243]
	s_add_u32 s26, s26, 0x8000
	s_cmp_eq_u32 s26, s32
	s_cselect_b32 s26, s27, s26
	v_mfma_f32_16x16x32_bf16 v[244:247], v[84:87], v[116:119], v[244:247]
	s_barrier
	v_add_u32_e32 v6, s33, v5
	ds_read_b128 v[72:75], v6 offset:0
	ds_read_b128 v[76:79], v6 offset:2048
	ds_read_b128 v[80:83], v6 offset:4096
	ds_read_b128 v[84:87], v6 offset:6144
	ds_read_b128 v[88:91], v4 offset:0
	ds_read_b128 v[92:95], v4 offset:2048
	ds_read_b128 v[96:99], v4 offset:4096
	ds_read_b128 v[100:103], v4 offset:6144
	ds_read_b128 v[104:107], v4 offset:8192
	ds_read_b128 v[108:111], v4 offset:10240
	ds_read_b128 v[112:115], v4 offset:12288
	ds_read_b128 v[116:119], v4 offset:14336
	s_waitcnt vmcnt(14)
	v_cvt_pk_bf16_f32 v40, v40, v41
	v_cvt_pk_bf16_f32 v41, v42, v43
	v_cvt_pk_bf16_f32 v44, v44, v45
	v_cvt_pk_bf16_f32 v45, v46, v47
	ds_write2st64_b64 v3, v[40:41], v[44:45] offset0:64 offset1:72
	s_waitcnt vmcnt(12)
	v_cvt_pk_bf16_f32 v48, v48, v49
	v_cvt_pk_bf16_f32 v49, v50, v51
	v_cvt_pk_bf16_f32 v52, v52, v53
	v_cvt_pk_bf16_f32 v53, v54, v55
	ds_write2st64_b64 v3, v[48:49], v[52:53] offset0:80 offset1:88
	s_waitcnt vmcnt(8)
	v_cvt_pk_bf16_f32 v56, v56, v57
	v_cvt_pk_bf16_f32 v57, v58, v59
	v_cvt_pk_bf16_f32 v60, v60, v61
	v_cvt_pk_bf16_f32 v61, v62, v63
	ds_write2st64_b64 v3, v[56:57], v[60:61] offset0:96 offset1:104
	s_waitcnt vmcnt(4)
	v_cvt_pk_bf16_f32 v64, v64, v65
	v_cvt_pk_bf16_f32 v65, v66, v67
	v_cvt_pk_bf16_f32 v68, v68, v69
	v_cvt_pk_bf16_f32 v69, v70, v71
	ds_write2st64_b64 v3, v[64:65], v[68:69] offset0:112 offset1:120
	s_waitcnt lgkmcnt(0)
	s_barrier
	v_mfma_f32_16x16x32_bf16 v[120:123], v[72:75], v[88:91], v[120:123]
	v_mfma_f32_16x16x32_bf16 v[124:127], v[76:79], v[88:91], v[124:127]
	v_mfma_f32_16x16x32_bf16 v[128:131], v[80:83], v[88:91], v[128:131]
	v_mfma_f32_16x16x32_bf16 v[132:135], v[84:87], v[88:91], v[132:135]
	v_mfma_f32_16x16x32_bf16 v[136:139], v[72:75], v[92:95], v[136:139]
	v_mfma_f32_16x16x32_bf16 v[140:143], v[76:79], v[92:95], v[140:143]
	v_mfma_f32_16x16x32_bf16 v[144:147], v[80:83], v[92:95], v[144:147]
	v_mfma_f32_16x16x32_bf16 v[148:151], v[84:87], v[92:95], v[148:151]
	v_mfma_f32_16x16x32_bf16 v[152:155], v[72:75], v[96:99], v[152:155]
	v_mfma_f32_16x16x32_bf16 v[156:159], v[76:79], v[96:99], v[156:159]
	v_mfma_f32_16x16x32_bf16 v[160:163], v[80:83], v[96:99], v[160:163]
	v_mfma_f32_16x16x32_bf16 v[164:167], v[84:87], v[96:99], v[164:167]
	v_mfma_f32_16x16x32_bf16 v[168:171], v[72:75], v[100:103], v[168:171]
	v_mfma_f32_16x16x32_bf16 v[172:175], v[76:79], v[100:103], v[172:175]
	v_mfma_f32_16x16x32_bf16 v[176:179], v[80:83], v[100:103], v[176:179]
	v_mfma_f32_16x16x32_bf16 v[180:183], v[84:87], v[100:103], v[180:183]
	v_mfma_f32_16x16x32_bf16 v[184:187], v[72:75], v[104:107], v[184:187]
	v_mfma_f32_16x16x32_bf16 v[188:191], v[76:79], v[104:107], v[188:191]
	v_mfma_f32_16x16x32_bf16 v[192:195], v[80:83], v[104:107], v[192:195]
	v_mfma_f32_16x16x32_bf16 v[196:199], v[84:87], v[104:107], v[196:199]
	v_mfma_f32_16x16x32_bf16 v[200:203], v[72:75], v[108:111], v[200:203]
	v_mfma_f32_16x16x32_bf16 v[204:207], v[76:79], v[108:111], v[204:207]
	v_mfma_f32_16x16x32_bf16 v[208:211], v[80:83], v[108:111], v[208:211]
	v_mfma_f32_16x16x32_bf16 v[212:215], v[84:87], v[108:111], v[212:215]
	v_mfma_f32_16x16x32_bf16 v[216:219], v[72:75], v[112:115], v[216:219]
	v_mfma_f32_16x16x32_bf16 v[220:223], v[76:79], v[112:115], v[220:223]
	v_mfma_f32_16x16x32_bf16 v[224:227], v[80:83], v[112:115], v[224:227]
	v_mfma_f32_16x16x32_bf16 v[228:231], v[84:87], v[112:115], v[228:231]
	v_mfma_f32_16x16x32_bf16 v[232:235], v[72:75], v[116:119], v[232:235]
	v_mfma_f32_16x16x32_bf16 v[236:239], v[76:79], v[116:119], v[236:239]
	v_mfma_f32_16x16x32_bf16 v[240:243], v[80:83], v[116:119], v[240:243]
	v_mfma_f32_16x16x32_bf16 v[244:247], v[84:87], v[116:119], v[244:247]
	s_barrier
	ds_read_b128 v[72:75], v6 offset:1024
	ds_read_b128 v[76:79], v6 offset:3072
	ds_read_b128 v[80:83], v6 offset:5120
	ds_read_b128 v[84:87], v6 offset:7168
	ds_read_b128 v[88:91], v4 offset:1024
	ds_read_b128 v[92:95], v4 offset:3072
	ds_read_b128 v[96:99], v4 offset:5120
	ds_read_b128 v[100:103], v4 offset:7168
	ds_read_b128 v[104:107], v4 offset:9216
	ds_read_b128 v[108:111], v4 offset:11264
	ds_read_b128 v[112:115], v4 offset:13312
	ds_read_b128 v[116:119], v4 offset:15360
	s_waitcnt vmcnt(0)
	s_waitcnt lgkmcnt(0)
	s_barrier
	v_mfma_f32_16x16x32_bf16 v[120:123], v[72:75], v[88:91], v[120:123]
	s_add_u32 s33, s33, 0x8000
	s_cmp_eq_u32 s33, 0x18000
	s_cselect_b32 s33, 0, s33
	s_add_u32 s25, s25, 1
	v_mfma_f32_16x16x32_bf16 v[124:127], v[76:79], v[88:91], v[124:127]
	v_mfma_f32_16x16x32_bf16 v[128:131], v[80:83], v[88:91], v[128:131]
	v_mfma_f32_16x16x32_bf16 v[132:135], v[84:87], v[88:91], v[132:135]
	v_mfma_f32_16x16x32_bf16 v[136:139], v[72:75], v[92:95], v[136:139]
	v_mfma_f32_16x16x32_bf16 v[140:143], v[76:79], v[92:95], v[140:143]
	v_mfma_f32_16x16x32_bf16 v[144:147], v[80:83], v[92:95], v[144:147]
	v_mfma_f32_16x16x32_bf16 v[148:151], v[84:87], v[92:95], v[148:151]
	v_mfma_f32_16x16x32_bf16 v[152:155], v[72:75], v[96:99], v[152:155]
	v_mfma_f32_16x16x32_bf16 v[156:159], v[76:79], v[96:99], v[156:159]
	v_mfma_f32_16x16x32_bf16 v[160:163], v[80:83], v[96:99], v[160:163]
	v_mfma_f32_16x16x32_bf16 v[164:167], v[84:87], v[96:99], v[164:167]
	v_mfma_f32_16x16x32_bf16 v[168:171], v[72:75], v[100:103], v[168:171]
	v_mfma_f32_16x16x32_bf16 v[172:175], v[76:79], v[100:103], v[172:175]
	v_mfma_f32_16x16x32_bf16 v[176:179], v[80:83], v[100:103], v[176:179]
	v_mfma_f32_16x16x32_bf16 v[180:183], v[84:87], v[100:103], v[180:183]
	v_mfma_f32_16x16x32_bf16 v[184:187], v[72:75], v[104:107], v[184:187]
	v_mfma_f32_16x16x32_bf16 v[188:191], v[76:79], v[104:107], v[188:191]
	v_mfma_f32_16x16x32_bf16 v[192:195], v[80:83], v[104:107], v[192:195]
	v_mfma_f32_16x16x32_bf16 v[196:199], v[84:87], v[104:107], v[196:199]
	v_mfma_f32_16x16x32_bf16 v[200:203], v[72:75], v[108:111], v[200:203]
	v_mfma_f32_16x16x32_bf16 v[204:207], v[76:79], v[108:111], v[204:207]
	v_mfma_f32_16x16x32_bf16 v[208:211], v[80:83], v[108:111], v[208:211]
	v_mfma_f32_16x16x32_bf16 v[212:215], v[84:87], v[108:111], v[212:215]
	v_mfma_f32_16x16x32_bf16 v[216:219], v[72:75], v[112:115], v[216:219]
	v_mfma_f32_16x16x32_bf16 v[220:223], v[76:79], v[112:115], v[220:223]
	v_mfma_f32_16x16x32_bf16 v[224:227], v[80:83], v[112:115], v[224:227]
	v_mfma_f32_16x16x32_bf16 v[228:231], v[84:87], v[112:115], v[228:231]
	v_mfma_f32_16x16x32_bf16 v[232:235], v[72:75], v[116:119], v[232:235]
	v_mfma_f32_16x16x32_bf16 v[236:239], v[76:79], v[116:119], v[236:239]
	v_mfma_f32_16x16x32_bf16 v[240:243], v[80:83], v[116:119], v[240:243]
	s_add_u32 s26, s26, 0x8000
	s_cmp_eq_u32 s26, s32
	s_cselect_b32 s26, s27, s26
	v_mfma_f32_16x16x32_bf16 v[244:247], v[84:87], v[116:119], v[244:247]
	s_barrier
	v_add_u32_e32 v6, s33, v5
	ds_read_b128 v[72:75], v6 offset:0
	ds_read_b128 v[76:79], v6 offset:2048
	ds_read_b128 v[80:83], v6 offset:4096
	ds_read_b128 v[84:87], v6 offset:6144
	ds_read_b128 v[88:91], v4 offset:32768
	ds_read_b128 v[92:95], v4 offset:34816
	ds_read_b128 v[96:99], v4 offset:36864
	ds_read_b128 v[100:103], v4 offset:38912
	ds_read_b128 v[104:107], v4 offset:40960
	ds_read_b128 v[108:111], v4 offset:43008
	ds_read_b128 v[112:115], v4 offset:45056
	ds_read_b128 v[116:119], v4 offset:47104
	s_waitcnt lgkmcnt(0)
	s_barrier
	v_mfma_f32_16x16x32_bf16 v[120:123], v[72:75], v[88:91], v[120:123]
	v_mfma_f32_16x16x32_bf16 v[124:127], v[76:79], v[88:91], v[124:127]
	v_mfma_f32_16x16x32_bf16 v[128:131], v[80:83], v[88:91], v[128:131]
	v_mfma_f32_16x16x32_bf16 v[132:135], v[84:87], v[88:91], v[132:135]
	v_mfma_f32_16x16x32_bf16 v[136:139], v[72:75], v[92:95], v[136:139]
	v_mfma_f32_16x16x32_bf16 v[140:143], v[76:79], v[92:95], v[140:143]
	v_mfma_f32_16x16x32_bf16 v[144:147], v[80:83], v[92:95], v[144:147]
	v_mfma_f32_16x16x32_bf16 v[148:151], v[84:87], v[92:95], v[148:151]
	v_mfma_f32_16x16x32_bf16 v[152:155], v[72:75], v[96:99], v[152:155]
	v_mfma_f32_16x16x32_bf16 v[156:159], v[76:79], v[96:99], v[156:159]
	v_mfma_f32_16x16x32_bf16 v[160:163], v[80:83], v[96:99], v[160:163]
	v_mfma_f32_16x16x32_bf16 v[164:167], v[84:87], v[96:99], v[164:167]
	v_mfma_f32_16x16x32_bf16 v[168:171], v[72:75], v[100:103], v[168:171]
	v_mfma_f32_16x16x32_bf16 v[172:175], v[76:79], v[100:103], v[172:175]
	v_mfma_f32_16x16x32_bf16 v[176:179], v[80:83], v[100:103], v[176:179]
	v_mfma_f32_16x16x32_bf16 v[180:183], v[84:87], v[100:103], v[180:183]
	v_mfma_f32_16x16x32_bf16 v[184:187], v[72:75], v[104:107], v[184:187]
	v_mfma_f32_16x16x32_bf16 v[188:191], v[76:79], v[104:107], v[188:191]
	v_mfma_f32_16x16x32_bf16 v[192:195], v[80:83], v[104:107], v[192:195]
	v_mfma_f32_16x16x32_bf16 v[196:199], v[84:87], v[104:107], v[196:199]
	v_mfma_f32_16x16x32_bf16 v[200:203], v[72:75], v[108:111], v[200:203]
	v_mfma_f32_16x16x32_bf16 v[204:207], v[76:79], v[108:111], v[204:207]
	v_mfma_f32_16x16x32_bf16 v[208:211], v[80:83], v[108:111], v[208:211]
	v_mfma_f32_16x16x32_bf16 v[212:215], v[84:87], v[108:111], v[212:215]
	v_mfma_f32_16x16x32_bf16 v[216:219], v[72:75], v[112:115], v[216:219]
	v_mfma_f32_16x16x32_bf16 v[220:223], v[76:79], v[112:115], v[220:223]
	v_mfma_f32_16x16x32_bf16 v[224:227], v[80:83], v[112:115], v[224:227]
	v_mfma_f32_16x16x32_bf16 v[228:231], v[84:87], v[112:115], v[228:231]
	v_mfma_f32_16x16x32_bf16 v[232:235], v[72:75], v[116:119], v[232:235]
	v_mfma_f32_16x16x32_bf16 v[236:239], v[76:79], v[116:119], v[236:239]
	v_mfma_f32_16x16x32_bf16 v[240:243], v[80:83], v[116:119], v[240:243]
	v_mfma_f32_16x16x32_bf16 v[244:247], v[84:87], v[116:119], v[244:247]
	s_barrier
	ds_read_b128 v[72:75], v6 offset:1024
	ds_read_b128 v[76:79], v6 offset:3072
	ds_read_b128 v[80:83], v6 offset:5120
	ds_read_b128 v[84:87], v6 offset:7168
	ds_read_b128 v[88:91], v4 offset:33792
	ds_read_b128 v[92:95], v4 offset:35840
	ds_read_b128 v[96:99], v4 offset:37888
	ds_read_b128 v[100:103], v4 offset:39936
	ds_read_b128 v[104:107], v4 offset:41984
	ds_read_b128 v[108:111], v4 offset:44032
	ds_read_b128 v[112:115], v4 offset:46080
	ds_read_b128 v[116:119], v4 offset:48128
	s_waitcnt lgkmcnt(0)
	s_barrier
	v_mfma_f32_16x16x32_bf16 v[120:123], v[72:75], v[88:91], v[120:123]
	s_add_u32 s33, s33, 0x8000
	s_cmp_eq_u32 s33, 0x18000
	s_cselect_b32 s33, 0, s33
	s_add_u32 s25, s25, 1
	v_mfma_f32_16x16x32_bf16 v[124:127], v[76:79], v[88:91], v[124:127]
	v_mfma_f32_16x16x32_bf16 v[128:131], v[80:83], v[88:91], v[128:131]
	v_mfma_f32_16x16x32_bf16 v[132:135], v[84:87], v[88:91], v[132:135]
	v_mfma_f32_16x16x32_bf16 v[136:139], v[72:75], v[92:95], v[136:139]
	v_mfma_f32_16x16x32_bf16 v[140:143], v[76:79], v[92:95], v[140:143]
	v_mfma_f32_16x16x32_bf16 v[144:147], v[80:83], v[92:95], v[144:147]
	v_mfma_f32_16x16x32_bf16 v[148:151], v[84:87], v[92:95], v[148:151]
	v_mfma_f32_16x16x32_bf16 v[152:155], v[72:75], v[96:99], v[152:155]
	v_mfma_f32_16x16x32_bf16 v[156:159], v[76:79], v[96:99], v[156:159]
	v_mfma_f32_16x16x32_bf16 v[160:163], v[80:83], v[96:99], v[160:163]
	v_mfma_f32_16x16x32_bf16 v[164:167], v[84:87], v[96:99], v[164:167]
	v_mfma_f32_16x16x32_bf16 v[168:171], v[72:75], v[100:103], v[168:171]
	v_mfma_f32_16x16x32_bf16 v[172:175], v[76:79], v[100:103], v[172:175]
	v_mfma_f32_16x16x32_bf16 v[176:179], v[80:83], v[100:103], v[176:179]
	v_mfma_f32_16x16x32_bf16 v[180:183], v[84:87], v[100:103], v[180:183]
	v_mfma_f32_16x16x32_bf16 v[184:187], v[72:75], v[104:107], v[184:187]
	v_mfma_f32_16x16x32_bf16 v[188:191], v[76:79], v[104:107], v[188:191]
	v_mfma_f32_16x16x32_bf16 v[192:195], v[80:83], v[104:107], v[192:195]
	v_mfma_f32_16x16x32_bf16 v[196:199], v[84:87], v[104:107], v[196:199]
	v_mfma_f32_16x16x32_bf16 v[200:203], v[72:75], v[108:111], v[200:203]
	v_mfma_f32_16x16x32_bf16 v[204:207], v[76:79], v[108:111], v[204:207]
	v_mfma_f32_16x16x32_bf16 v[208:211], v[80:83], v[108:111], v[208:211]
	v_mfma_f32_16x16x32_bf16 v[212:215], v[84:87], v[108:111], v[212:215]
	v_mfma_f32_16x16x32_bf16 v[216:219], v[72:75], v[112:115], v[216:219]
	v_mfma_f32_16x16x32_bf16 v[220:223], v[76:79], v[112:115], v[220:223]
	v_mfma_f32_16x16x32_bf16 v[224:227], v[80:83], v[112:115], v[224:227]
	v_mfma_f32_16x16x32_bf16 v[228:231], v[84:87], v[112:115], v[228:231]
	v_mfma_f32_16x16x32_bf16 v[232:235], v[72:75], v[116:119], v[232:235]
	v_mfma_f32_16x16x32_bf16 v[236:239], v[76:79], v[116:119], v[236:239]
	v_mfma_f32_16x16x32_bf16 v[240:243], v[80:83], v[116:119], v[240:243]
	s_add_u32 s26, s26, 0x8000
	s_cmp_eq_u32 s26, s32
	s_cselect_b32 s26, s27, s26
	v_mfma_f32_16x16x32_bf16 v[244:247], v[84:87], v[116:119], v[244:247]
	s_barrier
	s_cmp_ge_u32 s21, 4
	s_cbranch_scc1 .Lg_fin2
	s_barrier
